# baseline (speedup 1.0000x reference)
_Z9ssim_mainPKfS0_S0_Pf:
	v_readfirstlane_b32 s29, v0
	v_cmp_gt_u32_e32 vcc, 32, v0
	s_nop 1
	s_and_saveexec_b64 s[30:31], vcc
	v_mov_b32_e32 v1, 0x10000
	v_lshl_or_b32 v1, v0, 2, v1
	v_mov_b32_e32 v2, 0
	ds_write_b32 v1, v2
	s_or_b64 exec, exec, s[30:31]
	s_load_dwordx4 s[4:7], s[0:1], 0x0
	s_load_dwordx4 s[8:11], s[0:1], 0x10
	s_lshr_b32 s12, s29, 6
	s_mov_b32 s51, 0x44800000
	s_mov_b32 s38, 0
	s_mov_b32 s39, -1
	s_mov_b32 s92, -1
	s_mov_b32 s93, 0xffff
	s_mov_b32 s94, 0xffff
	s_mov_b32 s95, 0xffff
	v_and_b32_e32 v8, 63, v0
	v_and_b32_e32 v169, 15, v0
	v_bfe_u32 v164, v0, 4, 2
	v_lshlrev_b32_e32 v167, 3, v164
	v_xor_b32_e32 v168, 16, v167
	v_sub_u32_e32 v165, v167, v169
	v_sub_u32_e32 v166, v168, v169
	v_add_u32_e32 v172, 0, v165
	v_med3_i32 v172, v172, 0, 10
	v_lshlrev_b32_e32 v172, 2, v172
	v_add_u32_e32 v173, 1, v165
	v_med3_i32 v173, v173, 0, 10
	v_lshlrev_b32_e32 v173, 2, v173
	v_add_u32_e32 v174, 2, v165
	v_med3_i32 v174, v174, 0, 10
	v_lshlrev_b32_e32 v174, 2, v174
	v_add_u32_e32 v175, 3, v165
	v_med3_i32 v175, v175, 0, 10
	v_lshlrev_b32_e32 v175, 2, v175
	v_add_u32_e32 v176, 4, v165
	v_med3_i32 v176, v176, 0, 10
	v_lshlrev_b32_e32 v176, 2, v176
	v_add_u32_e32 v177, 5, v165
	v_med3_i32 v177, v177, 0, 10
	v_lshlrev_b32_e32 v177, 2, v177
	v_add_u32_e32 v178, 6, v165
	v_med3_i32 v178, v178, 0, 10
	v_lshlrev_b32_e32 v178, 2, v178
	v_add_u32_e32 v179, 7, v165
	v_med3_i32 v179, v179, 0, 10
	v_lshlrev_b32_e32 v179, 2, v179
	v_add_u32_e32 v180, 0, v166
	v_med3_i32 v180, v180, 0, 10
	v_lshlrev_b32_e32 v180, 2, v180
	v_add_u32_e32 v181, 1, v166
	v_med3_i32 v181, v181, 0, 10
	v_lshlrev_b32_e32 v181, 2, v181
	v_add_u32_e32 v182, 2, v166
	v_med3_i32 v182, v182, 0, 10
	v_lshlrev_b32_e32 v182, 2, v182
	v_add_u32_e32 v183, 3, v166
	v_med3_i32 v183, v183, 0, 10
	v_lshlrev_b32_e32 v183, 2, v183
	v_add_u32_e32 v184, 4, v166
	v_med3_i32 v184, v184, 0, 10
	v_lshlrev_b32_e32 v184, 2, v184
	v_add_u32_e32 v185, 5, v166
	v_med3_i32 v185, v185, 0, 10
	v_lshlrev_b32_e32 v185, 2, v185
	v_add_u32_e32 v186, 6, v166
	v_med3_i32 v186, v186, 0, 10
	v_lshlrev_b32_e32 v186, 2, v186
	v_add_u32_e32 v187, 7, v166
	v_med3_i32 v187, v187, 0, 10
	v_lshlrev_b32_e32 v187, 2, v187
	s_waitcnt lgkmcnt(0)
	global_load_dword v188, v172, s[8:9]
	global_load_dword v189, v173, s[8:9]
	global_load_dword v190, v174, s[8:9]
	global_load_dword v191, v175, s[8:9]
	global_load_dword v192, v176, s[8:9]
	global_load_dword v193, v177, s[8:9]
	global_load_dword v194, v178, s[8:9]
	global_load_dword v195, v179, s[8:9]
	global_load_dword v196, v180, s[8:9]
	global_load_dword v197, v181, s[8:9]
	global_load_dword v198, v182, s[8:9]
	global_load_dword v199, v183, s[8:9]
	global_load_dword v200, v184, s[8:9]
	global_load_dword v201, v185, s[8:9]
	global_load_dword v202, v186, s[8:9]
	global_load_dword v203, v187, s[8:9]
	s_load_dwordx8 s[40:47], s[8:9], 0x0
	s_load_dwordx2 s[48:49], s[8:9], 0x20
	s_load_dword s50, s[8:9], 0x28
	s_and_b32 s13, s2, 7
	s_lshl_b32 s13, s13, 5
	s_lshr_b32 s14, s2, 3
	s_add_u32 s13, s13, s14
	s_lshr_b32 s14, s13, 3
	s_and_b32 s15, s13, 7
	s_lshl_b32 s16, s14, 20
	s_lshl_b32 s17, s15, 17
	s_add_u32 s16, s16, s17
	s_lshl_b32 s17, s12, 8
	s_add_u32 s16, s16, s17
	s_add_u32 s18, s4, s16
	s_addc_u32 s19, s5, 0
	s_add_u32 s20, s6, s16
	s_addc_u32 s21, s7, 0
	s_mov_b32 s52, s18
	s_mov_b32 s53, s19
	s_add_u32 s54, s18, 0x1000
	s_addc_u32 s55, s19, 0
	s_add_u32 s56, s18, 0x2000
	s_addc_u32 s57, s19, 0
	s_add_u32 s58, s18, 0x3000
	s_addc_u32 s59, s19, 0
	s_add_u32 s60, s18, 0x10000
	s_addc_u32 s61, s19, 0
	s_add_u32 s62, s18, 0x11000
	s_addc_u32 s63, s19, 0
	s_add_u32 s64, s18, 0x12000
	s_addc_u32 s65, s19, 0
	s_add_u32 s66, s18, 0x13000
	s_addc_u32 s67, s19, 0
	s_mov_b32 s68, s20
	s_mov_b32 s69, s21
	s_add_u32 s70, s20, 0x1000
	s_addc_u32 s71, s21, 0
	s_add_u32 s72, s20, 0x2000
	s_addc_u32 s73, s21, 0
	s_add_u32 s74, s20, 0x3000
	s_addc_u32 s75, s21, 0
	s_add_u32 s76, s20, 0x10000
	s_addc_u32 s77, s21, 0
	s_add_u32 s78, s20, 0x11000
	s_addc_u32 s79, s21, 0
	s_add_u32 s80, s20, 0x12000
	s_addc_u32 s81, s21, 0
	s_add_u32 s82, s20, 0x13000
	s_addc_u32 s83, s21, 0
	s_cmp_eq_u32 s15, 7
	s_cselect_b32 s22, 0, 0x20000
	s_add_u32 s84, s18, s22
	s_addc_u32 s85, s19, 0
	s_add_u32 s86, s18, s22
	s_addc_u32 s87, s19, 0
	s_add_u32 s86, s86, 0x1000
	s_addc_u32 s87, s87, 0
	s_add_u32 s88, s20, s22
	s_addc_u32 s89, s21, 0
	s_add_u32 s90, s20, s22
	s_addc_u32 s91, s21, 0
	s_add_u32 s90, s90, 0x1000
	s_addc_u32 s91, s91, 0
	v_lshrrev_b32_e32 v167, 2, v169
	v_lshlrev_b32_e32 v167, 5, v167
	v_and_b32_e32 v168, 1, v169
	v_lshl_or_b32 v167, v168, 4, v167
	v_bfe_u32 v168, v169, 1, 1
	v_lshl_or_b32 v167, v168, 7, v167
	v_lshl_or_b32 v9, v164, 14, v167
	v_cmp_eq_u32_e32 vcc, 3, v164
	s_nop 1
	v_cndmask_b32_e64 v171, v164, 0, vcc
	v_and_b32_e32 v255, 2, v164
	v_and_b32_e32 v168, 1, v171
	v_lshl_or_b32 v23, v168, 14, v167
	v_lshrrev_b32_e32 v168, 1, v171
	v_lshl_or_b32 v23, v168, 13, v23
	v_and_b32_e32 v168, 1, v255
	v_lshl_or_b32 v170, v168, 14, v167
	v_lshrrev_b32_e32 v168, 1, v255
	v_lshl_or_b32 v170, v168, 13, v170
	global_load_dwordx4 v[36:39], v9, s[52:53] offset:0 nt
	global_load_dwordx4 v[40:43], v9, s[52:53] offset:2048 nt
	global_load_dwordx4 v[68:71], v9, s[68:69] offset:0 nt
	global_load_dwordx4 v[72:75], v9, s[68:69] offset:2048 nt
	global_load_dwordx4 v[44:47], v9, s[54:55] offset:0 nt
	global_load_dwordx4 v[48:51], v9, s[54:55] offset:2048 nt
	global_load_dwordx4 v[76:79], v9, s[70:71] offset:0 nt
	global_load_dwordx4 v[80:83], v9, s[70:71] offset:2048 nt
	global_load_dwordx4 v[52:55], v9, s[56:57] offset:0 nt
	global_load_dwordx4 v[56:59], v9, s[56:57] offset:2048 nt
	global_load_dwordx4 v[84:87], v9, s[72:73] offset:0 nt
	global_load_dwordx4 v[88:91], v9, s[72:73] offset:2048 nt
	global_load_dwordx4 v[60:63], v9, s[58:59] offset:0 nt
	global_load_dwordx4 v[64:67], v9, s[58:59] offset:2048 nt
	global_load_dwordx4 v[92:95], v9, s[74:75] offset:0 nt
	global_load_dwordx4 v[96:99], v9, s[74:75] offset:2048 nt
	global_load_dwordx4 v[100:103], v9, s[60:61] offset:0 nt
	global_load_dwordx4 v[104:107], v9, s[60:61] offset:2048 nt
	global_load_dwordx4 v[132:135], v9, s[76:77] offset:0 nt
	global_load_dwordx4 v[136:139], v9, s[76:77] offset:2048 nt
	global_load_dwordx4 v[108:111], v9, s[62:63] offset:0 nt
	global_load_dwordx4 v[112:115], v9, s[62:63] offset:2048 nt
	global_load_dwordx4 v[140:143], v9, s[78:79] offset:0 nt
	global_load_dwordx4 v[144:147], v9, s[78:79] offset:2048 nt
	global_load_dwordx4 v[116:119], v9, s[64:65] offset:0 nt
	global_load_dwordx4 v[120:123], v9, s[64:65] offset:2048 nt
	global_load_dwordx4 v[148:151], v9, s[80:81] offset:0 nt
	global_load_dwordx4 v[152:155], v9, s[80:81] offset:2048 nt
	global_load_dwordx4 v[124:127], v9, s[66:67] offset:0 nt
	global_load_dwordx4 v[128:131], v9, s[66:67] offset:2048 nt
	global_load_dwordx4 v[156:159], v9, s[82:83] offset:0 nt
	global_load_dwordx4 v[160:163], v9, s[82:83] offset:2048 nt
	s_lshl_b32 s96, s12, 13
	s_add_u32 s96, s96, 0x10400
	s_add_u32 m0, s96, 0x0
	s_nop 0
	global_load_lds_dwordx4 v23, s[84:85] offset:0 nt
	s_add_u32 m0, s96, 0xfffffc00
	s_nop 0
	global_load_lds_dwordx4 v23, s[84:85] offset:2048 nt
	s_add_u32 m0, s96, 0x1000
	s_nop 0
	global_load_lds_dwordx4 v23, s[88:89] offset:0 nt
	s_add_u32 m0, s96, 0xc00
	s_nop 0
	global_load_lds_dwordx4 v23, s[88:89] offset:2048 nt
	s_add_u32 m0, s96, 0x800
	s_nop 0
	global_load_lds_dwordx4 v170, s[86:87] offset:0 nt
	s_add_u32 m0, s96, 0x400
	s_nop 0
	global_load_lds_dwordx4 v170, s[86:87] offset:2048 nt
	s_add_u32 m0, s96, 0x1800
	s_nop 0
	global_load_lds_dwordx4 v170, s[90:91] offset:0 nt
	s_add_u32 m0, s96, 0x1400
	s_nop 0
	global_load_lds_dwordx4 v170, s[90:91] offset:2048 nt
	s_waitcnt lgkmcnt(0)
	v_mov_b32_e32 v229, 0x44800000
	v_fma_mixlo_f16 v228, s40, v229, 0
	v_cvt_f32_f16_e32 v228, v228
	v_cvt_f64_f32_e32 v[212:213], v228
	v_add_f64 v[212:213], v[212:213], 0
	v_fma_mixlo_f16 v228, s41, v229, 0
	v_cvt_f32_f16_e32 v228, v228
	v_cvt_f64_f32_e32 v[214:215], v228
	v_add_f64 v[212:213], v[212:213], v[214:215]
	v_fma_mixlo_f16 v228, s42, v229, 0
	v_cvt_f32_f16_e32 v228, v228
	v_cvt_f64_f32_e32 v[214:215], v228
	v_add_f64 v[212:213], v[212:213], v[214:215]
	v_fma_mixlo_f16 v228, s43, v229, 0
	v_cvt_f32_f16_e32 v228, v228
	v_cvt_f64_f32_e32 v[214:215], v228
	v_add_f64 v[212:213], v[212:213], v[214:215]
	v_fma_mixlo_f16 v228, s44, v229, 0
	v_cvt_f32_f16_e32 v228, v228
	v_cvt_f64_f32_e32 v[214:215], v228
	v_add_f64 v[212:213], v[212:213], v[214:215]
	v_fma_mixlo_f16 v228, s45, v229, 0
	v_cvt_f32_f16_e32 v228, v228
	v_cvt_f64_f32_e32 v[214:215], v228
	v_add_f64 v[212:213], v[212:213], v[214:215]
	v_fma_mixlo_f16 v228, s46, v229, 0
	v_cvt_f32_f16_e32 v228, v228
	v_cvt_f64_f32_e32 v[214:215], v228
	v_add_f64 v[212:213], v[212:213], v[214:215]
	v_fma_mixlo_f16 v228, s47, v229, 0
	v_cvt_f32_f16_e32 v228, v228
	v_cvt_f64_f32_e32 v[214:215], v228
	v_add_f64 v[212:213], v[212:213], v[214:215]
	v_fma_mixlo_f16 v228, s48, v229, 0
	v_cvt_f32_f16_e32 v228, v228
	v_cvt_f64_f32_e32 v[214:215], v228
	v_add_f64 v[212:213], v[212:213], v[214:215]
	v_fma_mixlo_f16 v228, s49, v229, 0
	v_cvt_f32_f16_e32 v228, v228
	v_cvt_f64_f32_e32 v[214:215], v228
	v_add_f64 v[212:213], v[212:213], v[214:215]
	v_fma_mixlo_f16 v228, s50, v229, 0
	v_cvt_f32_f16_e32 v228, v228
	v_cvt_f64_f32_e32 v[214:215], v228
	v_add_f64 v[212:213], v[212:213], v[214:215]
	v_mul_f64 v[212:213], v[212:213], v[212:213]
	v_mul_f64 v[216:217], v[212:213], 0.5
	v_add_f64 v[218:219], v[216:217], v[216:217]
	s_mov_b32 s36, 0xeb1c432d
	s_mov_b32 s37, 0x3f1a36e2
	v_mul_f64 v[220:221], v[212:213], s[36:37]
	v_mul_f64 v[222:223], v[216:217], v[218:219]
	v_fmac_f64_e32 v[222:223], v[212:213], v[220:221]
	v_add_f64 v[224:225], v[212:213], v[212:213]
	s_mov_b32 s36, 0x487fcb92
	s_mov_b32 s37, 0x3f4d7dbf
	v_mul_f64 v[226:227], v[212:213], s[36:37]
	v_cvt_f32_f64_e32 v0, v[226:227]
	v_mov_b32_e32 v1, v0
	v_mov_b32_e32 v2, v0
	v_mov_b32_e32 v3, v0
	v_cvt_f32_f64_e32 v10, v[218:219]
	v_cvt_f32_f64_e32 v11, v[222:223]
	v_cvt_f32_f64_e32 v12, v[212:213]
	v_cvt_f32_f64_e32 v13, v[224:225]
	v_mul_f64 v[226:227], v[212:213], v[226:227]
	v_cvt_f32_f64_e32 v14, v[226:227]
	v_lshlrev_b32_e32 v167, 2, v164
	s_cmp_eq_u32 s12, 0
	s_cselect_b32 s23, 6, 64
	v_add_u32_e32 v168, 0, v167
	v_cmp_gt_u32_e32 vcc, s23, v168
	s_nop 1
	v_cndmask_b32_e64 v15, 0, 1.0, vcc
	v_add_u32_e32 v168, 1, v167
	v_cmp_gt_u32_e32 vcc, s23, v168
	s_nop 1
	v_cndmask_b32_e64 v16, 0, 1.0, vcc
	v_add_u32_e32 v168, 2, v167
	v_cmp_gt_u32_e32 vcc, s23, v168
	s_nop 1
	v_cndmask_b32_e64 v17, 0, 1.0, vcc
	v_add_u32_e32 v168, 3, v167
	v_cmp_gt_u32_e32 vcc, s23, v168
	s_nop 1
	v_cndmask_b32_e64 v18, 0, 1.0, vcc
	v_and_b32_e32 v167, 31, v8
	v_lshlrev_b32_e32 v167, 4, v167
	s_lshl_b32 s24, s12, 11
	s_add_i32 s25, s12, 7
	s_and_b32 s25, s25, 7
	s_lshl_b32 s26, s25, 11
	v_or_b32_e32 v4, s24, v167
	v_or_b32_e32 v5, s26, v167
	s_lshl_b32 s27, s12, 2
	s_add_u32 s27, s27, 0x10000
	s_lshl_b32 s28, s25, 2
	s_add_u32 s28, s28, 0x10000
	v_mov_b32_e32 v6, s27
	v_mov_b32_e32 v7, s28
	v_mov_b32_e32 v19, 0
	v_mov_b32_e32 v20, 0
	v_mov_b32_e32 v21, 0
	v_mov_b32_e32 v22, 0
	s_waitcnt vmcnt(40)
	v_cmp_lt_u32_e64 s[32:33], 31, v8
	v_cmp_gt_u32_e64 s[34:35], 32, v8
	v_fma_mixlo_f16 v204, v188, s51, 0
	v_add_u32_e32 v167, 0, v165
	v_cmp_gt_u32_e32 vcc, 11, v167
	s_nop 1
	v_cndmask_b32_e32 v204, 0, v204, vcc
	v_fma_mixlo_f16 v205, v189, s51, 0
	v_add_u32_e32 v167, 1, v165
	v_cmp_gt_u32_e32 vcc, 11, v167
	s_nop 1
	v_cndmask_b32_e32 v205, 0, v205, vcc
	v_fma_mixlo_f16 v206, v190, s51, 0
	v_add_u32_e32 v167, 2, v165
	v_cmp_gt_u32_e32 vcc, 11, v167
	s_nop 1
	v_cndmask_b32_e32 v206, 0, v206, vcc
	v_fma_mixlo_f16 v207, v191, s51, 0
	v_add_u32_e32 v167, 3, v165
	v_cmp_gt_u32_e32 vcc, 11, v167
	s_nop 1
	v_cndmask_b32_e32 v207, 0, v207, vcc
	v_fma_mixlo_f16 v208, v192, s51, 0
	v_add_u32_e32 v167, 4, v165
	v_cmp_gt_u32_e32 vcc, 11, v167
	s_nop 1
	v_cndmask_b32_e32 v208, 0, v208, vcc
	v_fma_mixlo_f16 v209, v193, s51, 0
	v_add_u32_e32 v167, 5, v165
	v_cmp_gt_u32_e32 vcc, 11, v167
	s_nop 1
	v_cndmask_b32_e32 v209, 0, v209, vcc
	v_fma_mixlo_f16 v210, v194, s51, 0
	v_add_u32_e32 v167, 6, v165
	v_cmp_gt_u32_e32 vcc, 11, v167
	s_nop 1
	v_cndmask_b32_e32 v210, 0, v210, vcc
	v_fma_mixlo_f16 v211, v195, s51, 0
	v_add_u32_e32 v167, 7, v165
	v_cmp_gt_u32_e32 vcc, 11, v167
	s_nop 1
	v_cndmask_b32_e32 v211, 0, v211, vcc
	v_pack_b32_f16 v24, v204, v205
	v_pack_b32_f16 v25, v206, v207
	v_pack_b32_f16 v26, v208, v209
	v_pack_b32_f16 v27, v210, v211
	v_fma_mixlo_f16 v204, v196, s51, 0
	v_add_u32_e32 v167, 0, v166
	v_cmp_gt_u32_e32 vcc, 11, v167
	s_nop 1
	v_cndmask_b32_e32 v204, 0, v204, vcc
	v_fma_mixlo_f16 v205, v197, s51, 0
	v_add_u32_e32 v167, 1, v166
	v_cmp_gt_u32_e32 vcc, 11, v167
	s_nop 1
	v_cndmask_b32_e32 v205, 0, v205, vcc
	v_fma_mixlo_f16 v206, v198, s51, 0
	v_add_u32_e32 v167, 2, v166
	v_cmp_gt_u32_e32 vcc, 11, v167
	s_nop 1
	v_cndmask_b32_e32 v206, 0, v206, vcc
	v_fma_mixlo_f16 v207, v199, s51, 0
	v_add_u32_e32 v167, 3, v166
	v_cmp_gt_u32_e32 vcc, 11, v167
	s_nop 1
	v_cndmask_b32_e32 v207, 0, v207, vcc
	v_fma_mixlo_f16 v208, v200, s51, 0
	v_add_u32_e32 v167, 4, v166
	v_cmp_gt_u32_e32 vcc, 11, v167
	s_nop 1
	v_cndmask_b32_e32 v208, 0, v208, vcc
	v_fma_mixlo_f16 v209, v201, s51, 0
	v_add_u32_e32 v167, 5, v166
	v_cmp_gt_u32_e32 vcc, 11, v167
	s_nop 1
	v_cndmask_b32_e32 v209, 0, v209, vcc
	v_fma_mixlo_f16 v210, v202, s51, 0
	v_add_u32_e32 v167, 6, v166
	v_cmp_gt_u32_e32 vcc, 11, v167
	s_nop 1
	v_cndmask_b32_e32 v210, 0, v210, vcc
	v_fma_mixlo_f16 v211, v203, s51, 0
	v_add_u32_e32 v167, 7, v166
	v_cmp_gt_u32_e32 vcc, 11, v167
	s_nop 1
	v_cndmask_b32_e32 v211, 0, v211, vcc
	v_pack_b32_f16 v167, v204, v205
	v_cndmask_b32_e64 v28, 0, v167, s[32:33]
	v_cndmask_b32_e64 v32, 0, v167, s[34:35]
	v_pack_b32_f16 v167, v206, v207
	v_cndmask_b32_e64 v29, 0, v167, s[32:33]
	v_cndmask_b32_e64 v33, 0, v167, s[34:35]
	v_pack_b32_f16 v167, v208, v209
	v_cndmask_b32_e64 v30, 0, v167, s[32:33]
	v_cndmask_b32_e64 v34, 0, v167, s[34:35]
	v_pack_b32_f16 v167, v210, v211
	v_cndmask_b32_e64 v31, 0, v167, s[32:33]
	v_cndmask_b32_e64 v35, 0, v167, s[34:35]
	s_waitcnt lgkmcnt(0)
	s_barrier
	s_waitcnt vmcnt(36)
	v_cvt_pk_f16_f32 v164, v36, v40
	v_cvt_pk_f16_f32 v180, v68, v72
	v_pk_add_f16 v164, v164, -0.5 op_sel_hi:[1,0]
	v_pk_add_f16 v180, v180, -0.5 op_sel_hi:[1,0]
	v_pk_mul_f16 v196, v180, v180
	v_pk_mul_f16 v212, v164, v180
	v_pk_fma_f16 v196, v164, v164, v196
	v_cvt_pk_f16_f32 v168, v37, v41
	v_cvt_pk_f16_f32 v184, v69, v73
	v_pk_add_f16 v168, v168, -0.5 op_sel_hi:[1,0]
	v_pk_add_f16 v184, v184, -0.5 op_sel_hi:[1,0]
	v_pk_mul_f16 v200, v184, v184
	v_pk_mul_f16 v216, v168, v184
	v_pk_fma_f16 v200, v168, v168, v200
	v_cvt_pk_f16_f32 v172, v38, v42
	v_cvt_pk_f16_f32 v188, v70, v74
	v_pk_add_f16 v172, v172, -0.5 op_sel_hi:[1,0]
	v_pk_add_f16 v188, v188, -0.5 op_sel_hi:[1,0]
	v_pk_mul_f16 v204, v188, v188
	v_pk_mul_f16 v220, v172, v188
	v_pk_fma_f16 v204, v172, v172, v204
	v_cvt_pk_f16_f32 v176, v39, v43
	v_cvt_pk_f16_f32 v192, v71, v75
	v_pk_add_f16 v176, v176, -0.5 op_sel_hi:[1,0]
	v_pk_add_f16 v192, v192, -0.5 op_sel_hi:[1,0]
	v_pk_mul_f16 v208, v192, v192
	v_pk_mul_f16 v224, v176, v192
	v_pk_fma_f16 v208, v176, v176, v208
	s_waitcnt vmcnt(32)
	v_cvt_pk_f16_f32 v165, v44, v48
	v_cvt_pk_f16_f32 v181, v76, v80
	v_pk_add_f16 v165, v165, -0.5 op_sel_hi:[1,0]
	v_pk_add_f16 v181, v181, -0.5 op_sel_hi:[1,0]
	v_pk_mul_f16 v197, v181, v181
	v_pk_mul_f16 v213, v165, v181
	v_pk_fma_f16 v197, v165, v165, v197
	v_cvt_pk_f16_f32 v169, v45, v49
	v_cvt_pk_f16_f32 v185, v77, v81
	v_pk_add_f16 v169, v169, -0.5 op_sel_hi:[1,0]
	v_pk_add_f16 v185, v185, -0.5 op_sel_hi:[1,0]
	v_pk_mul_f16 v201, v185, v185
	v_pk_mul_f16 v217, v169, v185
	v_pk_fma_f16 v201, v169, v169, v201
	v_cvt_pk_f16_f32 v173, v46, v50
	v_cvt_pk_f16_f32 v189, v78, v82
	v_pk_add_f16 v173, v173, -0.5 op_sel_hi:[1,0]
	v_pk_add_f16 v189, v189, -0.5 op_sel_hi:[1,0]
	v_pk_mul_f16 v205, v189, v189
	v_pk_mul_f16 v221, v173, v189
	v_pk_fma_f16 v205, v173, v173, v205
	v_cvt_pk_f16_f32 v177, v47, v51
	v_cvt_pk_f16_f32 v193, v79, v83
	v_pk_add_f16 v177, v177, -0.5 op_sel_hi:[1,0]
	v_pk_add_f16 v193, v193, -0.5 op_sel_hi:[1,0]
	v_pk_mul_f16 v209, v193, v193
	v_pk_mul_f16 v225, v177, v193
	v_pk_fma_f16 v209, v177, v177, v209
	s_waitcnt vmcnt(28)
	v_cvt_pk_f16_f32 v166, v52, v56
	v_cvt_pk_f16_f32 v182, v84, v88
	v_pk_add_f16 v166, v166, -0.5 op_sel_hi:[1,0]
	v_pk_add_f16 v182, v182, -0.5 op_sel_hi:[1,0]
	v_pk_mul_f16 v198, v182, v182
	v_pk_mul_f16 v214, v166, v182
	v_pk_fma_f16 v198, v166, v166, v198
	v_cvt_pk_f16_f32 v170, v53, v57
	v_cvt_pk_f16_f32 v186, v85, v89
	v_pk_add_f16 v170, v170, -0.5 op_sel_hi:[1,0]
	v_pk_add_f16 v186, v186, -0.5 op_sel_hi:[1,0]
	v_pk_mul_f16 v202, v186, v186
	v_pk_mul_f16 v218, v170, v186
	v_pk_fma_f16 v202, v170, v170, v202
	v_cvt_pk_f16_f32 v174, v54, v58
	v_cvt_pk_f16_f32 v190, v86, v90
	v_pk_add_f16 v174, v174, -0.5 op_sel_hi:[1,0]
	v_pk_add_f16 v190, v190, -0.5 op_sel_hi:[1,0]
	v_pk_mul_f16 v206, v190, v190
	v_pk_mul_f16 v222, v174, v190
	v_pk_fma_f16 v206, v174, v174, v206
	v_cvt_pk_f16_f32 v178, v55, v59
	v_cvt_pk_f16_f32 v194, v87, v91
	v_pk_add_f16 v178, v178, -0.5 op_sel_hi:[1,0]
	v_pk_add_f16 v194, v194, -0.5 op_sel_hi:[1,0]
	v_pk_mul_f16 v210, v194, v194
	v_pk_mul_f16 v226, v178, v194
	v_pk_fma_f16 v210, v178, v178, v210
	s_waitcnt vmcnt(24)
	v_cvt_pk_f16_f32 v167, v60, v64
	v_cvt_pk_f16_f32 v183, v92, v96
	v_pk_add_f16 v167, v167, -0.5 op_sel_hi:[1,0]
	v_pk_add_f16 v183, v183, -0.5 op_sel_hi:[1,0]
	v_pk_mul_f16 v199, v183, v183
	v_pk_mul_f16 v215, v167, v183
	v_pk_fma_f16 v199, v167, v167, v199
	v_cvt_pk_f16_f32 v171, v61, v65
	v_cvt_pk_f16_f32 v187, v93, v97
	v_pk_add_f16 v171, v171, -0.5 op_sel_hi:[1,0]
	v_pk_add_f16 v187, v187, -0.5 op_sel_hi:[1,0]
	v_pk_mul_f16 v203, v187, v187
	v_pk_mul_f16 v219, v171, v187
	v_pk_fma_f16 v203, v171, v171, v203
	v_cvt_pk_f16_f32 v175, v62, v66
	v_cvt_pk_f16_f32 v191, v94, v98
	v_pk_add_f16 v175, v175, -0.5 op_sel_hi:[1,0]
	v_pk_add_f16 v191, v191, -0.5 op_sel_hi:[1,0]
	v_pk_mul_f16 v207, v191, v191
	v_pk_mul_f16 v223, v175, v191
	v_pk_fma_f16 v207, v175, v175, v207
	v_cvt_pk_f16_f32 v179, v63, v67
	v_cvt_pk_f16_f32 v195, v95, v99
	v_pk_add_f16 v179, v179, -0.5 op_sel_hi:[1,0]
	v_pk_add_f16 v195, v195, -0.5 op_sel_hi:[1,0]
	v_pk_mul_f16 v211, v195, v195
	v_pk_mul_f16 v227, v179, v195
	v_pk_fma_f16 v211, v179, v179, v211
	v_mfma_f32_16x16x32_f16 v[68:71], v[164:167], v[24:27], 0
	v_mfma_f32_16x16x32_f16 v[72:75], v[168:171], v[24:27], 0
	v_mfma_f32_16x16x32_f16 v[76:79], v[172:175], v[24:27], 0
	v_mfma_f32_16x16x32_f16 v[80:83], v[176:179], v[24:27], 0
	v_mfma_f32_16x16x32_f16 v[84:87], v[180:183], v[24:27], 0
	v_mfma_f32_16x16x32_f16 v[88:91], v[184:187], v[24:27], 0
	v_mfma_f32_16x16x32_f16 v[92:95], v[188:191], v[24:27], 0
	v_mfma_f32_16x16x32_f16 v[96:99], v[192:195], v[24:27], 0
	s_nop 1
	v_cvt_pk_f16_f32 v36, v68, v72
	s_nop 0
	v_cvt_pk_f16_f32 v37, v76, v80
	v_cvt_pk_f16_f32 v38, v69, v73
	v_cvt_pk_f16_f32 v39, v77, v81
	v_cvt_pk_f16_f32 v40, v70, v74
	v_cvt_pk_f16_f32 v41, v78, v82
	v_cvt_pk_f16_f32 v42, v71, v75
	v_cvt_pk_f16_f32 v43, v79, v83
	v_mfma_f32_16x16x32_f16 v[68:71], v[196:199], v[24:27], 0
	v_mfma_f32_16x16x32_f16 v[72:75], v[200:203], v[24:27], 0
	v_mfma_f32_16x16x32_f16 v[76:79], v[204:207], v[24:27], 0
	v_mfma_f32_16x16x32_f16 v[80:83], v[208:211], v[24:27], 0
	v_cvt_pk_f16_f32 v44, v84, v88
	v_cvt_pk_f16_f32 v45, v92, v96
	v_cvt_pk_f16_f32 v46, v85, v89
	v_cvt_pk_f16_f32 v47, v93, v97
	v_cvt_pk_f16_f32 v48, v86, v90
	v_cvt_pk_f16_f32 v49, v94, v98
	v_cvt_pk_f16_f32 v50, v87, v91
	v_cvt_pk_f16_f32 v51, v95, v99
	v_mfma_f32_16x16x32_f16 v[84:87], v[212:215], v[24:27], 0
	v_mfma_f32_16x16x32_f16 v[88:91], v[216:219], v[24:27], 0
	v_mfma_f32_16x16x32_f16 v[92:95], v[220:223], v[24:27], 0
	v_mfma_f32_16x16x32_f16 v[96:99], v[224:227], v[24:27], 0
	v_cvt_pk_f16_f32 v52, v68, v72
	v_cvt_pk_f16_f32 v53, v76, v80
	v_cvt_pk_f16_f32 v54, v69, v73
	v_cvt_pk_f16_f32 v55, v77, v81
	v_cvt_pk_f16_f32 v56, v70, v74
	v_cvt_pk_f16_f32 v57, v78, v82
	v_cvt_pk_f16_f32 v58, v71, v75
	v_cvt_pk_f16_f32 v59, v79, v83
	v_cvt_pk_f16_f32 v60, v84, v88
	v_cvt_pk_f16_f32 v61, v92, v96
	v_cvt_pk_f16_f32 v62, v85, v89
	v_cvt_pk_f16_f32 v63, v93, v97
	v_cvt_pk_f16_f32 v64, v86, v90
	v_cvt_pk_f16_f32 v65, v94, v98
	v_cvt_pk_f16_f32 v66, v87, v91
	v_cvt_pk_f16_f32 v67, v95, v99
	s_mov_b64 exec, s[38:39]
	ds_write_b128 v4, v[40:43] offset:0
	ds_write_b128 v4, v[48:51] offset:512
	ds_write_b128 v4, v[56:59] offset:1024
	ds_write_b128 v4, v[64:67] offset:1536
	s_mov_b64 exec, -1
	v_mfma_f32_16x16x32_f16 v[68:71], v[24:27], v[36:39], 0
	v_mfma_f32_16x16x32_f16 v[72:75], v[24:27], v[44:47], 0
	v_mfma_f32_16x16x32_f16 v[76:79], v[24:27], v[52:55], v[0:3]
	v_mfma_f32_16x16x32_f16 v[80:83], v[24:27], v[60:63], 0
	v_mfma_f32_16x16x32_f16 v[84:87], v[28:31], v[36:39], 0
	v_mfma_f32_16x16x32_f16 v[88:91], v[28:31], v[44:47], 0
	v_mfma_f32_16x16x32_f16 v[92:95], v[28:31], v[52:55], v[0:3]
	v_mfma_f32_16x16x32_f16 v[96:99], v[28:31], v[60:63], 0
	v_mfma_f32_16x16x32_f16 v[84:87], v[32:35], v[40:43], v[84:87]
	v_mfma_f32_16x16x32_f16 v[88:91], v[32:35], v[48:51], v[88:91]
	v_mfma_f32_16x16x32_f16 v[92:95], v[32:35], v[56:59], v[92:95]
	v_mfma_f32_16x16x32_f16 v[96:99], v[32:35], v[64:67], v[96:99]
	s_waitcnt lgkmcnt(0)
	ds_write_b32 v6, v6 offset:0
	ds_read_b32 v9, v7 offset:0
	v_mul_f32_e32 v244, v68, v72
	v_mul_f32_e32 v250, v69, v73
	v_mul_f32_e64 v245, -v72, v72
	v_mul_f32_e64 v251, -v73, v73
	v_add_f32_e32 v246, v68, v72
	v_add_f32_e32 v252, v69, v73
	v_fma_f32 v245, -v68, v68, v245
	v_fma_f32 v251, -v69, v69, v251
	v_fma_f32 v247, v10, v246, v11
	v_fma_f32 v253, v10, v252, v11
	v_fma_f32 v246, v13, v80, v14
	v_fma_f32 v252, v13, v81, v14
	v_fma_f32 v248, v12, v76, v245
	v_fma_f32 v254, v12, v77, v251
	v_fma_f32 v249, 2.0, v244, v247
	v_fma_f32 v255, 2.0, v250, v253
	v_sub_f32_e32 v247, v247, v245
	v_sub_f32_e32 v253, v253, v251
	v_fma_f32 v246, -2.0, v244, v246
	v_fma_f32 v252, -2.0, v250, v252
	v_mul_f32_e32 v247, v247, v248
	v_mul_f32_e32 v253, v253, v254
	v_rcp_f32_e32 v247, v247
	v_rcp_f32_e32 v253, v253
	v_mul_f32_e32 v249, v249, v246
	v_mul_f32_e32 v255, v255, v252
	v_fma_f32 v19, v249, v247, v19
	v_fma_f32 v19, v255, v253, v19
	v_mul_f32_e32 v244, v70, v74
	v_mul_f32_e32 v250, v71, v75
	v_mul_f32_e64 v245, -v74, v74
	v_mul_f32_e64 v251, -v75, v75
	v_add_f32_e32 v246, v70, v74
	v_add_f32_e32 v252, v71, v75
	v_fma_f32 v245, -v70, v70, v245
	v_fma_f32 v251, -v71, v71, v251
	v_fma_f32 v247, v10, v246, v11
	v_fma_f32 v253, v10, v252, v11
	v_fma_f32 v246, v13, v82, v14
	v_fma_f32 v252, v13, v83, v14
	v_fma_f32 v248, v12, v78, v245
	v_fma_f32 v254, v12, v79, v251
	v_fma_f32 v249, 2.0, v244, v247
	v_fma_f32 v255, 2.0, v250, v253
	v_sub_f32_e32 v247, v247, v245
	v_sub_f32_e32 v253, v253, v251
	v_fma_f32 v246, -2.0, v244, v246
	v_fma_f32 v252, -2.0, v250, v252
	v_mul_f32_e32 v247, v247, v248
	v_mul_f32_e32 v253, v253, v254
	v_rcp_f32_e32 v247, v247
	v_rcp_f32_e32 v253, v253
	v_mul_f32_e32 v249, v249, v246
	v_mul_f32_e32 v255, v255, v252
	v_fma_f32 v20, v249, v247, v20
	v_fma_f32 v20, v255, v253, v20
	v_mfma_f32_16x16x32_f16 v[68:71], v[24:27], v[40:43], 0
	v_mfma_f32_16x16x32_f16 v[72:75], v[24:27], v[48:51], 0
	v_mfma_f32_16x16x32_f16 v[76:79], v[24:27], v[56:59], v[0:3]
	v_mfma_f32_16x16x32_f16 v[80:83], v[24:27], v[64:67], 0
	s_waitcnt lgkmcnt(0)
	v_cmp_ne_u32_e32 vcc, 0, v9
	s_cbranch_vccnz .Lq_go_0
.Lq_spin_0:
	s_sleep 1
	ds_read_b32 v9, v7 offset:0
	s_waitcnt lgkmcnt(0)
	v_cmp_eq_u32_e32 vcc, 0, v9
	s_cbranch_vccnz .Lq_spin_0
.Lq_go_0:
	ds_read_b128 v[228:231], v5 offset:0
	ds_read_b128 v[232:235], v5 offset:512
	ds_read_b128 v[236:239], v5 offset:1024
	ds_read_b128 v[240:243], v5 offset:1536
	v_mul_f32_e32 v244, v84, v88
	v_mul_f32_e32 v250, v85, v89
	v_mul_f32_e64 v245, -v88, v88
	v_mul_f32_e64 v251, -v89, v89
	v_add_f32_e32 v246, v84, v88
	v_add_f32_e32 v252, v85, v89
	v_fma_f32 v245, -v84, v84, v245
	v_fma_f32 v251, -v85, v85, v251
	v_fma_f32 v247, v10, v246, v11
	v_fma_f32 v253, v10, v252, v11
	v_fma_f32 v246, v13, v96, v14
	v_fma_f32 v252, v13, v97, v14
	v_fma_f32 v248, v12, v92, v245
	v_fma_f32 v254, v12, v93, v251
	v_fma_f32 v249, 2.0, v244, v247
	v_fma_f32 v255, 2.0, v250, v253
	v_sub_f32_e32 v247, v247, v245
	v_sub_f32_e32 v253, v253, v251
	v_fma_f32 v246, -2.0, v244, v246
	v_fma_f32 v252, -2.0, v250, v252
	v_mul_f32_e32 v247, v247, v248
	v_mul_f32_e32 v253, v253, v254
	v_rcp_f32_e32 v247, v247
	v_rcp_f32_e32 v253, v253
	v_mul_f32_e32 v249, v249, v246
	v_mul_f32_e32 v255, v255, v252
	v_fma_f32 v19, v249, v247, v19
	v_fma_f32 v19, v255, v253, v19
	v_mul_f32_e32 v244, v86, v90
	v_mul_f32_e32 v250, v87, v91
	v_mul_f32_e64 v245, -v90, v90
	v_mul_f32_e64 v251, -v91, v91
	v_add_f32_e32 v246, v86, v90
	v_add_f32_e32 v252, v87, v91
	v_fma_f32 v245, -v86, v86, v245
	v_fma_f32 v251, -v87, v87, v251
	v_fma_f32 v247, v10, v246, v11
	v_fma_f32 v253, v10, v252, v11
	v_fma_f32 v246, v13, v98, v14
	v_fma_f32 v252, v13, v99, v14
	v_fma_f32 v248, v12, v94, v245
	v_fma_f32 v254, v12, v95, v251
	v_fma_f32 v249, 2.0, v244, v247
	v_fma_f32 v255, 2.0, v250, v253
	v_sub_f32_e32 v247, v247, v245
	v_sub_f32_e32 v253, v253, v251
	v_fma_f32 v246, -2.0, v244, v246
	v_fma_f32 v252, -2.0, v250, v252
	v_mul_f32_e32 v247, v247, v248
	v_mul_f32_e32 v253, v253, v254
	v_rcp_f32_e32 v247, v247
	v_rcp_f32_e32 v253, v253
	v_mul_f32_e32 v249, v249, v246
	v_mul_f32_e32 v255, v255, v252
	v_fma_f32 v20, v249, v247, v20
	v_fma_f32 v20, v255, v253, v20
	s_waitcnt lgkmcnt(0)
	v_mfma_f32_16x16x32_f16 v[84:87], v[28:31], v[228:231], 0
	v_mfma_f32_16x16x32_f16 v[88:91], v[28:31], v[232:235], 0
	v_mfma_f32_16x16x32_f16 v[92:95], v[28:31], v[236:239], v[0:3]
	v_mfma_f32_16x16x32_f16 v[96:99], v[28:31], v[240:243], 0
	v_mfma_f32_16x16x32_f16 v[84:87], v[32:35], v[36:39], v[84:87]
	v_mfma_f32_16x16x32_f16 v[88:91], v[32:35], v[44:47], v[88:91]
	v_mfma_f32_16x16x32_f16 v[92:95], v[32:35], v[52:55], v[92:95]
	v_mfma_f32_16x16x32_f16 v[96:99], v[32:35], v[60:63], v[96:99]
	v_mul_f32_e32 v244, v68, v72
	v_mul_f32_e32 v250, v69, v73
	v_mul_f32_e64 v245, -v72, v72
	v_mul_f32_e64 v251, -v73, v73
	v_add_f32_e32 v246, v68, v72
	v_add_f32_e32 v252, v69, v73
	v_fma_f32 v245, -v68, v68, v245
	v_fma_f32 v251, -v69, v69, v251
	v_fma_f32 v247, v10, v246, v11
	v_fma_f32 v253, v10, v252, v11
	v_fma_f32 v246, v13, v80, v14
	v_fma_f32 v252, v13, v81, v14
	v_fma_f32 v248, v12, v76, v245
	v_fma_f32 v254, v12, v77, v251
	v_fma_f32 v249, 2.0, v244, v247
	v_fma_f32 v255, 2.0, v250, v253
	v_sub_f32_e32 v247, v247, v245
	v_sub_f32_e32 v253, v253, v251
	v_fma_f32 v246, -2.0, v244, v246
	v_fma_f32 v252, -2.0, v250, v252
	v_mul_f32_e32 v247, v247, v248
	v_mul_f32_e32 v253, v253, v254
	v_rcp_f32_e32 v247, v247
	v_rcp_f32_e32 v253, v253
	v_mul_f32_e32 v249, v249, v246
	v_mul_f32_e32 v255, v255, v252
	v_fma_f32 v19, v249, v247, v19
	v_fma_f32 v19, v255, v253, v19
	v_mul_f32_e32 v244, v70, v74
	v_mul_f32_e32 v250, v71, v75
	v_mul_f32_e64 v245, -v74, v74
	v_mul_f32_e64 v251, -v75, v75
	v_add_f32_e32 v246, v70, v74
	v_add_f32_e32 v252, v71, v75
	v_fma_f32 v245, -v70, v70, v245
	v_fma_f32 v251, -v71, v71, v251
	v_fma_f32 v247, v10, v246, v11
	v_fma_f32 v253, v10, v252, v11
	v_fma_f32 v246, v13, v82, v14
	v_fma_f32 v252, v13, v83, v14
	v_fma_f32 v248, v12, v78, v245
	v_fma_f32 v254, v12, v79, v251
	v_fma_f32 v249, 2.0, v244, v247
	v_fma_f32 v255, 2.0, v250, v253
	v_sub_f32_e32 v247, v247, v245
	v_sub_f32_e32 v253, v253, v251
	v_fma_f32 v246, -2.0, v244, v246
	v_fma_f32 v252, -2.0, v250, v252
	v_mul_f32_e32 v247, v247, v248
	v_mul_f32_e32 v253, v253, v254
	v_rcp_f32_e32 v247, v247
	v_rcp_f32_e32 v253, v253
	v_mul_f32_e32 v249, v249, v246
	v_mul_f32_e32 v255, v255, v252
	v_fma_f32 v20, v249, v247, v20
	v_fma_f32 v20, v255, v253, v20
	v_mul_f32_e32 v244, v84, v88
	v_mul_f32_e32 v250, v85, v89
	v_mul_f32_e64 v245, -v88, v88
	v_mul_f32_e64 v251, -v89, v89
	v_add_f32_e32 v246, v84, v88
	v_add_f32_e32 v252, v85, v89
	v_fma_f32 v245, -v84, v84, v245
	v_fma_f32 v251, -v85, v85, v251
	v_fma_f32 v247, v10, v246, v11
	v_fma_f32 v253, v10, v252, v11
	v_fma_f32 v246, v13, v96, v14
	v_fma_f32 v252, v13, v97, v14
	v_fma_f32 v248, v12, v92, v245
	v_fma_f32 v254, v12, v93, v251
	v_fma_f32 v249, 2.0, v244, v247
	v_fma_f32 v255, 2.0, v250, v253
	v_sub_f32_e32 v247, v247, v245
	v_sub_f32_e32 v253, v253, v251
	v_fma_f32 v246, -2.0, v244, v246
	v_fma_f32 v252, -2.0, v250, v252
	v_mul_f32_e32 v247, v247, v248
	v_mul_f32_e32 v253, v253, v254
	v_rcp_f32_e32 v247, v247
	v_rcp_f32_e32 v253, v253
	v_mul_f32_e32 v249, v249, v246
	v_mul_f32_e32 v255, v255, v252
	v_mul_f32_e32 v249, v249, v247
	v_mul_f32_e32 v255, v255, v253
	v_fma_f32 v19, v249, v15, v19
	v_fma_f32 v19, v255, v16, v19
	v_mul_f32_e32 v244, v86, v90
	v_mul_f32_e32 v250, v87, v91
	v_mul_f32_e64 v245, -v90, v90
	v_mul_f32_e64 v251, -v91, v91
	v_add_f32_e32 v246, v86, v90
	v_add_f32_e32 v252, v87, v91
	v_fma_f32 v245, -v86, v86, v245
	v_fma_f32 v251, -v87, v87, v251
	v_fma_f32 v247, v10, v246, v11
	v_fma_f32 v253, v10, v252, v11
	v_fma_f32 v246, v13, v98, v14
	v_fma_f32 v252, v13, v99, v14
	v_fma_f32 v248, v12, v94, v245
	v_fma_f32 v254, v12, v95, v251
	v_fma_f32 v249, 2.0, v244, v247
	v_fma_f32 v255, 2.0, v250, v253
	v_sub_f32_e32 v247, v247, v245
	v_sub_f32_e32 v253, v253, v251
	v_fma_f32 v246, -2.0, v244, v246
	v_fma_f32 v252, -2.0, v250, v252
	v_mul_f32_e32 v247, v247, v248
	v_mul_f32_e32 v253, v253, v254
	v_rcp_f32_e32 v247, v247
	v_rcp_f32_e32 v253, v253
	v_mul_f32_e32 v249, v249, v246
	v_mul_f32_e32 v255, v255, v252
	v_mul_f32_e32 v249, v249, v247
	v_mul_f32_e32 v255, v255, v253
	v_fma_f32 v20, v249, v17, v20
	v_fma_f32 v20, v255, v18, v20
	s_waitcnt vmcnt(20)
	v_cvt_pk_f16_f32 v36, v100, v104
	v_cvt_pk_f16_f32 v52, v132, v136
	v_pk_add_f16 v36, v36, -0.5 op_sel_hi:[1,0]
	v_pk_add_f16 v52, v52, -0.5 op_sel_hi:[1,0]
	v_pk_mul_f16 v68, v52, v52
	v_pk_mul_f16 v84, v36, v52
	v_pk_fma_f16 v68, v36, v36, v68
	v_cvt_pk_f16_f32 v40, v101, v105
	v_cvt_pk_f16_f32 v56, v133, v137
	v_pk_add_f16 v40, v40, -0.5 op_sel_hi:[1,0]
	v_pk_add_f16 v56, v56, -0.5 op_sel_hi:[1,0]
	v_pk_mul_f16 v72, v56, v56
	v_pk_mul_f16 v88, v40, v56
	v_pk_fma_f16 v72, v40, v40, v72
	v_cvt_pk_f16_f32 v44, v102, v106
	v_cvt_pk_f16_f32 v60, v134, v138
	v_pk_add_f16 v44, v44, -0.5 op_sel_hi:[1,0]
	v_pk_add_f16 v60, v60, -0.5 op_sel_hi:[1,0]
	v_pk_mul_f16 v76, v60, v60
	v_pk_mul_f16 v92, v44, v60
	v_pk_fma_f16 v76, v44, v44, v76
	v_cvt_pk_f16_f32 v48, v103, v107
	v_cvt_pk_f16_f32 v64, v135, v139
	v_pk_add_f16 v48, v48, -0.5 op_sel_hi:[1,0]
	v_pk_add_f16 v64, v64, -0.5 op_sel_hi:[1,0]
	v_pk_mul_f16 v80, v64, v64
	v_pk_mul_f16 v96, v48, v64
	v_pk_fma_f16 v80, v48, v48, v80
	s_waitcnt vmcnt(16)
	v_cvt_pk_f16_f32 v37, v108, v112
	v_cvt_pk_f16_f32 v53, v140, v144
	v_pk_add_f16 v37, v37, -0.5 op_sel_hi:[1,0]
	v_pk_add_f16 v53, v53, -0.5 op_sel_hi:[1,0]
	v_pk_mul_f16 v69, v53, v53
	v_pk_mul_f16 v85, v37, v53
	v_pk_fma_f16 v69, v37, v37, v69
	v_cvt_pk_f16_f32 v41, v109, v113
	v_cvt_pk_f16_f32 v57, v141, v145
	v_pk_add_f16 v41, v41, -0.5 op_sel_hi:[1,0]
	v_pk_add_f16 v57, v57, -0.5 op_sel_hi:[1,0]
	v_pk_mul_f16 v73, v57, v57
	v_pk_mul_f16 v89, v41, v57
	v_pk_fma_f16 v73, v41, v41, v73
	v_cvt_pk_f16_f32 v45, v110, v114
	v_cvt_pk_f16_f32 v61, v142, v146
	v_pk_add_f16 v45, v45, -0.5 op_sel_hi:[1,0]
	v_pk_add_f16 v61, v61, -0.5 op_sel_hi:[1,0]
	v_pk_mul_f16 v77, v61, v61
	v_pk_mul_f16 v93, v45, v61
	v_pk_fma_f16 v77, v45, v45, v77
	v_cvt_pk_f16_f32 v49, v111, v115
	v_cvt_pk_f16_f32 v65, v143, v147
	v_pk_add_f16 v49, v49, -0.5 op_sel_hi:[1,0]
	v_pk_add_f16 v65, v65, -0.5 op_sel_hi:[1,0]
	v_pk_mul_f16 v81, v65, v65
	v_pk_mul_f16 v97, v49, v65
	v_pk_fma_f16 v81, v49, v49, v81
	s_waitcnt vmcnt(12)
	v_cvt_pk_f16_f32 v38, v116, v120
	v_cvt_pk_f16_f32 v54, v148, v152
	v_pk_add_f16 v38, v38, -0.5 op_sel_hi:[1,0]
	v_pk_add_f16 v54, v54, -0.5 op_sel_hi:[1,0]
	v_pk_mul_f16 v70, v54, v54
	v_pk_mul_f16 v86, v38, v54
	v_pk_fma_f16 v70, v38, v38, v70
	v_cvt_pk_f16_f32 v42, v117, v121
	v_cvt_pk_f16_f32 v58, v149, v153
	v_pk_add_f16 v42, v42, -0.5 op_sel_hi:[1,0]
	v_pk_add_f16 v58, v58, -0.5 op_sel_hi:[1,0]
	v_pk_mul_f16 v74, v58, v58
	v_pk_mul_f16 v90, v42, v58
	v_pk_fma_f16 v74, v42, v42, v74
	v_cvt_pk_f16_f32 v46, v118, v122
	v_cvt_pk_f16_f32 v62, v150, v154
	v_pk_add_f16 v46, v46, -0.5 op_sel_hi:[1,0]
	v_pk_add_f16 v62, v62, -0.5 op_sel_hi:[1,0]
	v_pk_mul_f16 v78, v62, v62
	v_pk_mul_f16 v94, v46, v62
	v_pk_fma_f16 v78, v46, v46, v78
	v_cvt_pk_f16_f32 v50, v119, v123
	v_cvt_pk_f16_f32 v66, v151, v155
	v_pk_add_f16 v50, v50, -0.5 op_sel_hi:[1,0]
	v_pk_add_f16 v66, v66, -0.5 op_sel_hi:[1,0]
	v_pk_mul_f16 v82, v66, v66
	v_pk_mul_f16 v98, v50, v66
	v_pk_fma_f16 v82, v50, v50, v82
	s_waitcnt vmcnt(8)
	v_cvt_pk_f16_f32 v39, v124, v128
	v_cvt_pk_f16_f32 v55, v156, v160
	v_pk_add_f16 v39, v39, -0.5 op_sel_hi:[1,0]
	v_pk_add_f16 v55, v55, -0.5 op_sel_hi:[1,0]
	v_pk_mul_f16 v71, v55, v55
	v_pk_mul_f16 v87, v39, v55
	v_pk_fma_f16 v71, v39, v39, v71
	v_cvt_pk_f16_f32 v43, v125, v129
	v_cvt_pk_f16_f32 v59, v157, v161
	v_pk_add_f16 v43, v43, -0.5 op_sel_hi:[1,0]
	v_pk_add_f16 v59, v59, -0.5 op_sel_hi:[1,0]
	v_pk_mul_f16 v75, v59, v59
	v_pk_mul_f16 v91, v43, v59
	v_pk_fma_f16 v75, v43, v43, v75
	v_cvt_pk_f16_f32 v47, v126, v130
	v_cvt_pk_f16_f32 v63, v158, v162
	v_pk_add_f16 v47, v47, -0.5 op_sel_hi:[1,0]
	v_pk_add_f16 v63, v63, -0.5 op_sel_hi:[1,0]
	v_pk_mul_f16 v79, v63, v63
	v_pk_mul_f16 v95, v47, v63
	v_pk_fma_f16 v79, v47, v47, v79
	v_cvt_pk_f16_f32 v51, v127, v131
	v_cvt_pk_f16_f32 v67, v159, v163
	v_pk_add_f16 v51, v51, -0.5 op_sel_hi:[1,0]
	v_pk_add_f16 v67, v67, -0.5 op_sel_hi:[1,0]
	v_pk_mul_f16 v83, v67, v67
	v_pk_mul_f16 v99, v51, v67
	v_pk_fma_f16 v83, v51, v51, v83
	v_mfma_f32_16x16x32_f16 v[132:135], v[164:167], v[28:31], 0
	v_mfma_f32_16x16x32_f16 v[136:139], v[168:171], v[28:31], 0
	v_mfma_f32_16x16x32_f16 v[140:143], v[172:175], v[28:31], 0
	v_mfma_f32_16x16x32_f16 v[144:147], v[176:179], v[28:31], 0
	v_mfma_f32_16x16x32_f16 v[132:135], v[36:39], v[32:35], v[132:135]
	v_mfma_f32_16x16x32_f16 v[136:139], v[40:43], v[32:35], v[136:139]
	v_mfma_f32_16x16x32_f16 v[140:143], v[44:47], v[32:35], v[140:143]
	v_mfma_f32_16x16x32_f16 v[144:147], v[48:51], v[32:35], v[144:147]
	v_mfma_f32_16x16x32_f16 v[148:151], v[180:183], v[28:31], 0
	v_mfma_f32_16x16x32_f16 v[152:155], v[184:187], v[28:31], 0
	v_mfma_f32_16x16x32_f16 v[156:159], v[188:191], v[28:31], 0
	v_mfma_f32_16x16x32_f16 v[160:163], v[192:195], v[28:31], 0
	v_mfma_f32_16x16x32_f16 v[148:151], v[52:55], v[32:35], v[148:151]
	v_mfma_f32_16x16x32_f16 v[152:155], v[56:59], v[32:35], v[152:155]
	v_mfma_f32_16x16x32_f16 v[156:159], v[60:63], v[32:35], v[156:159]
	v_mfma_f32_16x16x32_f16 v[160:163], v[64:67], v[32:35], v[160:163]
	v_cvt_pk_f16_f32 v100, v132, v136
	v_cvt_pk_f16_f32 v101, v140, v144
	v_cvt_pk_f16_f32 v102, v133, v137
	v_cvt_pk_f16_f32 v103, v141, v145
	v_cvt_pk_f16_f32 v104, v134, v138
	v_cvt_pk_f16_f32 v105, v142, v146
	v_cvt_pk_f16_f32 v106, v135, v139
	v_cvt_pk_f16_f32 v107, v143, v147
	v_mfma_f32_16x16x32_f16 v[132:135], v[196:199], v[28:31], 0
	v_mfma_f32_16x16x32_f16 v[136:139], v[200:203], v[28:31], 0
	v_mfma_f32_16x16x32_f16 v[140:143], v[204:207], v[28:31], 0
	v_mfma_f32_16x16x32_f16 v[144:147], v[208:211], v[28:31], 0
	v_mfma_f32_16x16x32_f16 v[132:135], v[68:71], v[32:35], v[132:135]
	v_mfma_f32_16x16x32_f16 v[136:139], v[72:75], v[32:35], v[136:139]
	v_mfma_f32_16x16x32_f16 v[140:143], v[76:79], v[32:35], v[140:143]
	v_mfma_f32_16x16x32_f16 v[144:147], v[80:83], v[32:35], v[144:147]
	v_cvt_pk_f16_f32 v108, v148, v152
	v_cvt_pk_f16_f32 v109, v156, v160
	v_cvt_pk_f16_f32 v110, v149, v153
	v_cvt_pk_f16_f32 v111, v157, v161
	v_cvt_pk_f16_f32 v112, v150, v154
	v_cvt_pk_f16_f32 v113, v158, v162
	v_cvt_pk_f16_f32 v114, v151, v155
	v_cvt_pk_f16_f32 v115, v159, v163
	v_mfma_f32_16x16x32_f16 v[148:151], v[212:215], v[28:31], 0
	v_mfma_f32_16x16x32_f16 v[152:155], v[216:219], v[28:31], 0
	v_mfma_f32_16x16x32_f16 v[156:159], v[220:223], v[28:31], 0
	v_mfma_f32_16x16x32_f16 v[160:163], v[224:227], v[28:31], 0
	v_mfma_f32_16x16x32_f16 v[148:151], v[84:87], v[32:35], v[148:151]
	v_mfma_f32_16x16x32_f16 v[152:155], v[88:91], v[32:35], v[152:155]
	v_mfma_f32_16x16x32_f16 v[156:159], v[92:95], v[32:35], v[156:159]
	v_mfma_f32_16x16x32_f16 v[160:163], v[96:99], v[32:35], v[160:163]
	v_cvt_pk_f16_f32 v116, v132, v136
	v_cvt_pk_f16_f32 v117, v140, v144
	v_cvt_pk_f16_f32 v118, v133, v137
	v_cvt_pk_f16_f32 v119, v141, v145
	v_cvt_pk_f16_f32 v120, v134, v138
	v_cvt_pk_f16_f32 v121, v142, v146
	v_cvt_pk_f16_f32 v122, v135, v139
	v_cvt_pk_f16_f32 v123, v143, v147
	v_cvt_pk_f16_f32 v124, v148, v152
	v_cvt_pk_f16_f32 v125, v156, v160
	v_cvt_pk_f16_f32 v126, v149, v153
	v_cvt_pk_f16_f32 v127, v157, v161
	v_cvt_pk_f16_f32 v128, v150, v154
	v_cvt_pk_f16_f32 v129, v158, v162
	v_cvt_pk_f16_f32 v130, v151, v155
	v_cvt_pk_f16_f32 v131, v159, v163
	s_mov_b64 exec, s[38:39]
	ds_write_b128 v4, v[104:107] offset:16384
	ds_write_b128 v4, v[112:115] offset:16896
	ds_write_b128 v4, v[120:123] offset:17408
	ds_write_b128 v4, v[128:131] offset:17920
	s_mov_b64 exec, -1
	v_mfma_f32_16x16x32_f16 v[132:135], v[24:27], v[100:103], 0
	v_mfma_f32_16x16x32_f16 v[136:139], v[24:27], v[108:111], 0
	v_mfma_f32_16x16x32_f16 v[140:143], v[24:27], v[116:119], v[0:3]
	v_mfma_f32_16x16x32_f16 v[144:147], v[24:27], v[124:127], 0
	v_mfma_f32_16x16x32_f16 v[148:151], v[28:31], v[100:103], 0
	v_mfma_f32_16x16x32_f16 v[152:155], v[28:31], v[108:111], 0
	v_mfma_f32_16x16x32_f16 v[156:159], v[28:31], v[116:119], v[0:3]
	v_mfma_f32_16x16x32_f16 v[160:163], v[28:31], v[124:127], 0
	v_mfma_f32_16x16x32_f16 v[148:151], v[32:35], v[104:107], v[148:151]
	v_mfma_f32_16x16x32_f16 v[152:155], v[32:35], v[112:115], v[152:155]
	v_mfma_f32_16x16x32_f16 v[156:159], v[32:35], v[120:123], v[156:159]
	v_mfma_f32_16x16x32_f16 v[160:163], v[32:35], v[128:131], v[160:163]
	s_waitcnt lgkmcnt(0)
	ds_write_b32 v6, v6 offset:32
	ds_read_b32 v9, v7 offset:32
	v_mul_f32_e32 v244, v132, v136
	v_mul_f32_e32 v250, v133, v137
	v_mul_f32_e64 v245, -v136, v136
	v_mul_f32_e64 v251, -v137, v137
	v_add_f32_e32 v246, v132, v136
	v_add_f32_e32 v252, v133, v137
	v_fma_f32 v245, -v132, v132, v245
	v_fma_f32 v251, -v133, v133, v251
	v_fma_f32 v247, v10, v246, v11
	v_fma_f32 v253, v10, v252, v11
	v_fma_f32 v246, v13, v144, v14
	v_fma_f32 v252, v13, v145, v14
	v_fma_f32 v248, v12, v140, v245
	v_fma_f32 v254, v12, v141, v251
	v_fma_f32 v249, 2.0, v244, v247
	v_fma_f32 v255, 2.0, v250, v253
	v_sub_f32_e32 v247, v247, v245
	v_sub_f32_e32 v253, v253, v251
	v_fma_f32 v246, -2.0, v244, v246
	v_fma_f32 v252, -2.0, v250, v252
	v_mul_f32_e32 v247, v247, v248
	v_mul_f32_e32 v253, v253, v254
	v_rcp_f32_e32 v247, v247
	v_rcp_f32_e32 v253, v253
	v_mul_f32_e32 v249, v249, v246
	v_mul_f32_e32 v255, v255, v252
	v_fma_f32 v19, v249, v247, v19
	v_fma_f32 v19, v255, v253, v19
	v_mul_f32_e32 v244, v134, v138
	v_mul_f32_e32 v250, v135, v139
	v_mul_f32_e64 v245, -v138, v138
	v_mul_f32_e64 v251, -v139, v139
	v_add_f32_e32 v246, v134, v138
	v_add_f32_e32 v252, v135, v139
	v_fma_f32 v245, -v134, v134, v245
	v_fma_f32 v251, -v135, v135, v251
	v_fma_f32 v247, v10, v246, v11
	v_fma_f32 v253, v10, v252, v11
	v_fma_f32 v246, v13, v146, v14
	v_fma_f32 v252, v13, v147, v14
	v_fma_f32 v248, v12, v142, v245
	v_fma_f32 v254, v12, v143, v251
	v_fma_f32 v249, 2.0, v244, v247
	v_fma_f32 v255, 2.0, v250, v253
	v_sub_f32_e32 v247, v247, v245
	v_sub_f32_e32 v253, v253, v251
	v_fma_f32 v246, -2.0, v244, v246
	v_fma_f32 v252, -2.0, v250, v252
	v_mul_f32_e32 v247, v247, v248
	v_mul_f32_e32 v253, v253, v254
	v_rcp_f32_e32 v247, v247
	v_rcp_f32_e32 v253, v253
	v_mul_f32_e32 v249, v249, v246
	v_mul_f32_e32 v255, v255, v252
	v_fma_f32 v20, v249, v247, v20
	v_fma_f32 v20, v255, v253, v20
	v_mfma_f32_16x16x32_f16 v[132:135], v[24:27], v[104:107], 0
	v_mfma_f32_16x16x32_f16 v[136:139], v[24:27], v[112:115], 0
	v_mfma_f32_16x16x32_f16 v[140:143], v[24:27], v[120:123], v[0:3]
	v_mfma_f32_16x16x32_f16 v[144:147], v[24:27], v[128:131], 0
	s_waitcnt lgkmcnt(0)
	v_cmp_ne_u32_e32 vcc, 0, v9
	s_cbranch_vccnz .Lq_go_1
.Lq_spin_1:
	s_sleep 1
	ds_read_b32 v9, v7 offset:32
	s_waitcnt lgkmcnt(0)
	v_cmp_eq_u32_e32 vcc, 0, v9
	s_cbranch_vccnz .Lq_spin_1
.Lq_go_1:
	ds_read_b128 v[228:231], v5 offset:16384
	ds_read_b128 v[232:235], v5 offset:16896
	ds_read_b128 v[236:239], v5 offset:17408
	ds_read_b128 v[240:243], v5 offset:17920
	v_mul_f32_e32 v244, v148, v152
	v_mul_f32_e32 v250, v149, v153
	v_mul_f32_e64 v245, -v152, v152
	v_mul_f32_e64 v251, -v153, v153
	v_add_f32_e32 v246, v148, v152
	v_add_f32_e32 v252, v149, v153
	v_fma_f32 v245, -v148, v148, v245
	v_fma_f32 v251, -v149, v149, v251
	v_fma_f32 v247, v10, v246, v11
	v_fma_f32 v253, v10, v252, v11
	v_fma_f32 v246, v13, v160, v14
	v_fma_f32 v252, v13, v161, v14
	v_fma_f32 v248, v12, v156, v245
	v_fma_f32 v254, v12, v157, v251
	v_fma_f32 v249, 2.0, v244, v247
	v_fma_f32 v255, 2.0, v250, v253
	v_sub_f32_e32 v247, v247, v245
	v_sub_f32_e32 v253, v253, v251
	v_fma_f32 v246, -2.0, v244, v246
	v_fma_f32 v252, -2.0, v250, v252
	v_mul_f32_e32 v247, v247, v248
	v_mul_f32_e32 v253, v253, v254
	v_rcp_f32_e32 v247, v247
	v_rcp_f32_e32 v253, v253
	v_mul_f32_e32 v249, v249, v246
	v_mul_f32_e32 v255, v255, v252
	v_fma_f32 v19, v249, v247, v19
	v_fma_f32 v19, v255, v253, v19
	v_mul_f32_e32 v244, v150, v154
	v_mul_f32_e32 v250, v151, v155
	v_mul_f32_e64 v245, -v154, v154
	v_mul_f32_e64 v251, -v155, v155
	v_add_f32_e32 v246, v150, v154
	v_add_f32_e32 v252, v151, v155
	v_fma_f32 v245, -v150, v150, v245
	v_fma_f32 v251, -v151, v151, v251
	v_fma_f32 v247, v10, v246, v11
	v_fma_f32 v253, v10, v252, v11
	v_fma_f32 v246, v13, v162, v14
	v_fma_f32 v252, v13, v163, v14
	v_fma_f32 v248, v12, v158, v245
	v_fma_f32 v254, v12, v159, v251
	v_fma_f32 v249, 2.0, v244, v247
	v_fma_f32 v255, 2.0, v250, v253
	v_sub_f32_e32 v247, v247, v245
	v_sub_f32_e32 v253, v253, v251
	v_fma_f32 v246, -2.0, v244, v246
	v_fma_f32 v252, -2.0, v250, v252
	v_mul_f32_e32 v247, v247, v248
	v_mul_f32_e32 v253, v253, v254
	v_rcp_f32_e32 v247, v247
	v_rcp_f32_e32 v253, v253
	v_mul_f32_e32 v249, v249, v246
	v_mul_f32_e32 v255, v255, v252
	v_fma_f32 v20, v249, v247, v20
	v_fma_f32 v20, v255, v253, v20
	s_waitcnt lgkmcnt(0)
	v_mfma_f32_16x16x32_f16 v[148:151], v[28:31], v[228:231], 0
	v_mfma_f32_16x16x32_f16 v[152:155], v[28:31], v[232:235], 0
	v_mfma_f32_16x16x32_f16 v[156:159], v[28:31], v[236:239], v[0:3]
	v_mfma_f32_16x16x32_f16 v[160:163], v[28:31], v[240:243], 0
	v_mfma_f32_16x16x32_f16 v[148:151], v[32:35], v[100:103], v[148:151]
	v_mfma_f32_16x16x32_f16 v[152:155], v[32:35], v[108:111], v[152:155]
	v_mfma_f32_16x16x32_f16 v[156:159], v[32:35], v[116:119], v[156:159]
	v_mfma_f32_16x16x32_f16 v[160:163], v[32:35], v[124:127], v[160:163]
	v_mul_f32_e32 v244, v132, v136
	v_mul_f32_e32 v250, v133, v137
	v_mul_f32_e64 v245, -v136, v136
	v_mul_f32_e64 v251, -v137, v137
	v_add_f32_e32 v246, v132, v136
	v_add_f32_e32 v252, v133, v137
	v_fma_f32 v245, -v132, v132, v245
	v_fma_f32 v251, -v133, v133, v251
	v_fma_f32 v247, v10, v246, v11
	v_fma_f32 v253, v10, v252, v11
	v_fma_f32 v246, v13, v144, v14
	v_fma_f32 v252, v13, v145, v14
	v_fma_f32 v248, v12, v140, v245
	v_fma_f32 v254, v12, v141, v251
	v_fma_f32 v249, 2.0, v244, v247
	v_fma_f32 v255, 2.0, v250, v253
	v_sub_f32_e32 v247, v247, v245
	v_sub_f32_e32 v253, v253, v251
	v_fma_f32 v246, -2.0, v244, v246
	v_fma_f32 v252, -2.0, v250, v252
	v_mul_f32_e32 v247, v247, v248
	v_mul_f32_e32 v253, v253, v254
	v_rcp_f32_e32 v247, v247
	v_rcp_f32_e32 v253, v253
	v_mul_f32_e32 v249, v249, v246
	v_mul_f32_e32 v255, v255, v252
	v_fma_f32 v19, v249, v247, v19
	v_fma_f32 v19, v255, v253, v19
	v_mul_f32_e32 v244, v134, v138
	v_mul_f32_e32 v250, v135, v139
	v_mul_f32_e64 v245, -v138, v138
	v_mul_f32_e64 v251, -v139, v139
	v_add_f32_e32 v246, v134, v138
	v_add_f32_e32 v252, v135, v139
	v_fma_f32 v245, -v134, v134, v245
	v_fma_f32 v251, -v135, v135, v251
	v_fma_f32 v247, v10, v246, v11
	v_fma_f32 v253, v10, v252, v11
	v_fma_f32 v246, v13, v146, v14
	v_fma_f32 v252, v13, v147, v14
	v_fma_f32 v248, v12, v142, v245
	v_fma_f32 v254, v12, v143, v251
	v_fma_f32 v249, 2.0, v244, v247
	v_fma_f32 v255, 2.0, v250, v253
	v_sub_f32_e32 v247, v247, v245
	v_sub_f32_e32 v253, v253, v251
	v_fma_f32 v246, -2.0, v244, v246
	v_fma_f32 v252, -2.0, v250, v252
	v_mul_f32_e32 v247, v247, v248
	v_mul_f32_e32 v253, v253, v254
	v_rcp_f32_e32 v247, v247
	v_rcp_f32_e32 v253, v253
	v_mul_f32_e32 v249, v249, v246
	v_mul_f32_e32 v255, v255, v252
	v_fma_f32 v20, v249, v247, v20
	v_fma_f32 v20, v255, v253, v20
	v_mul_f32_e32 v244, v148, v152
	v_mul_f32_e32 v250, v149, v153
	v_mul_f32_e64 v245, -v152, v152
	v_mul_f32_e64 v251, -v153, v153
	v_add_f32_e32 v246, v148, v152
	v_add_f32_e32 v252, v149, v153
	v_fma_f32 v245, -v148, v148, v245
	v_fma_f32 v251, -v149, v149, v251
	v_fma_f32 v247, v10, v246, v11
	v_fma_f32 v253, v10, v252, v11
	v_fma_f32 v246, v13, v160, v14
	v_fma_f32 v252, v13, v161, v14
	v_fma_f32 v248, v12, v156, v245
	v_fma_f32 v254, v12, v157, v251
	v_fma_f32 v249, 2.0, v244, v247
	v_fma_f32 v255, 2.0, v250, v253
	v_sub_f32_e32 v247, v247, v245
	v_sub_f32_e32 v253, v253, v251
	v_fma_f32 v246, -2.0, v244, v246
	v_fma_f32 v252, -2.0, v250, v252
	v_mul_f32_e32 v247, v247, v248
	v_mul_f32_e32 v253, v253, v254
	v_rcp_f32_e32 v247, v247
	v_rcp_f32_e32 v253, v253
	v_mul_f32_e32 v249, v249, v246
	v_mul_f32_e32 v255, v255, v252
	v_mul_f32_e32 v249, v249, v247
	v_mul_f32_e32 v255, v255, v253
	v_fma_f32 v19, v249, v15, v19
	v_fma_f32 v19, v255, v16, v19
	v_mul_f32_e32 v244, v150, v154
	v_mul_f32_e32 v250, v151, v155
	v_mul_f32_e64 v245, -v154, v154
	v_mul_f32_e64 v251, -v155, v155
	v_add_f32_e32 v246, v150, v154
	v_add_f32_e32 v252, v151, v155
	v_fma_f32 v245, -v150, v150, v245
	v_fma_f32 v251, -v151, v151, v251
	v_fma_f32 v247, v10, v246, v11
	v_fma_f32 v253, v10, v252, v11
	v_fma_f32 v246, v13, v162, v14
	v_fma_f32 v252, v13, v163, v14
	v_fma_f32 v248, v12, v158, v245
	v_fma_f32 v254, v12, v159, v251
	v_fma_f32 v249, 2.0, v244, v247
	v_fma_f32 v255, 2.0, v250, v253
	v_sub_f32_e32 v247, v247, v245
	v_sub_f32_e32 v253, v253, v251
	v_fma_f32 v246, -2.0, v244, v246
	v_fma_f32 v252, -2.0, v250, v252
	v_mul_f32_e32 v247, v247, v248
	v_mul_f32_e32 v253, v253, v254
	v_rcp_f32_e32 v247, v247
	v_rcp_f32_e32 v253, v253
	v_mul_f32_e32 v249, v249, v246
	v_mul_f32_e32 v255, v255, v252
	v_mul_f32_e32 v249, v249, v247
	v_mul_f32_e32 v255, v255, v253
	v_fma_f32 v20, v249, v17, v20
	v_fma_f32 v20, v255, v18, v20
	v_mfma_f32_16x16x32_f16 v[132:135], v[36:39], v[24:27], 0
	v_mfma_f32_16x16x32_f16 v[136:139], v[40:43], v[24:27], 0
	v_mfma_f32_16x16x32_f16 v[140:143], v[44:47], v[24:27], 0
	v_mfma_f32_16x16x32_f16 v[144:147], v[48:51], v[24:27], 0
	v_mfma_f32_16x16x32_f16 v[148:151], v[52:55], v[24:27], 0
	v_mfma_f32_16x16x32_f16 v[152:155], v[56:59], v[24:27], 0
	v_mfma_f32_16x16x32_f16 v[156:159], v[60:63], v[24:27], 0
	v_mfma_f32_16x16x32_f16 v[160:163], v[64:67], v[24:27], 0
	s_nop 1
	v_cvt_pk_f16_f32 v100, v132, v136
	s_nop 0
	v_cvt_pk_f16_f32 v101, v140, v144
	v_cvt_pk_f16_f32 v102, v133, v137
	v_cvt_pk_f16_f32 v103, v141, v145
	v_cvt_pk_f16_f32 v104, v134, v138
	v_cvt_pk_f16_f32 v105, v142, v146
	v_cvt_pk_f16_f32 v106, v135, v139
	v_cvt_pk_f16_f32 v107, v143, v147
	v_mfma_f32_16x16x32_f16 v[132:135], v[68:71], v[24:27], 0
	v_mfma_f32_16x16x32_f16 v[136:139], v[72:75], v[24:27], 0
	v_mfma_f32_16x16x32_f16 v[140:143], v[76:79], v[24:27], 0
	v_mfma_f32_16x16x32_f16 v[144:147], v[80:83], v[24:27], 0
	v_cvt_pk_f16_f32 v108, v148, v152
	v_cvt_pk_f16_f32 v109, v156, v160
	v_cvt_pk_f16_f32 v110, v149, v153
	v_cvt_pk_f16_f32 v111, v157, v161
	v_cvt_pk_f16_f32 v112, v150, v154
	v_cvt_pk_f16_f32 v113, v158, v162
	v_cvt_pk_f16_f32 v114, v151, v155
	v_cvt_pk_f16_f32 v115, v159, v163
	v_mfma_f32_16x16x32_f16 v[148:151], v[84:87], v[24:27], 0
	v_mfma_f32_16x16x32_f16 v[152:155], v[88:91], v[24:27], 0
	v_mfma_f32_16x16x32_f16 v[156:159], v[92:95], v[24:27], 0
	v_mfma_f32_16x16x32_f16 v[160:163], v[96:99], v[24:27], 0
	v_cvt_pk_f16_f32 v116, v132, v136
	v_cvt_pk_f16_f32 v117, v140, v144
	v_cvt_pk_f16_f32 v118, v133, v137
	v_cvt_pk_f16_f32 v119, v141, v145
	v_cvt_pk_f16_f32 v120, v134, v138
	v_cvt_pk_f16_f32 v121, v142, v146
	v_cvt_pk_f16_f32 v122, v135, v139
	v_cvt_pk_f16_f32 v123, v143, v147
	v_cvt_pk_f16_f32 v124, v148, v152
	v_cvt_pk_f16_f32 v125, v156, v160
	v_cvt_pk_f16_f32 v126, v149, v153
	v_cvt_pk_f16_f32 v127, v157, v161
	v_cvt_pk_f16_f32 v128, v150, v154
	v_cvt_pk_f16_f32 v129, v158, v162
	v_cvt_pk_f16_f32 v130, v151, v155
	v_cvt_pk_f16_f32 v131, v159, v163
	s_mov_b64 exec, s[38:39]
	ds_write_b128 v4, v[104:107] offset:32768
	ds_write_b128 v4, v[112:115] offset:33280
	ds_write_b128 v4, v[120:123] offset:33792
	ds_write_b128 v4, v[128:131] offset:34304
	s_mov_b64 exec, -1
	v_mfma_f32_16x16x32_f16 v[132:135], v[24:27], v[100:103], 0
	v_mfma_f32_16x16x32_f16 v[136:139], v[24:27], v[108:111], 0
	v_mfma_f32_16x16x32_f16 v[140:143], v[24:27], v[116:119], v[0:3]
	v_mfma_f32_16x16x32_f16 v[144:147], v[24:27], v[124:127], 0
	v_mfma_f32_16x16x32_f16 v[148:151], v[28:31], v[100:103], 0
	v_mfma_f32_16x16x32_f16 v[152:155], v[28:31], v[108:111], 0
	v_mfma_f32_16x16x32_f16 v[156:159], v[28:31], v[116:119], v[0:3]
	v_mfma_f32_16x16x32_f16 v[160:163], v[28:31], v[124:127], 0
	v_mfma_f32_16x16x32_f16 v[148:151], v[32:35], v[104:107], v[148:151]
	v_mfma_f32_16x16x32_f16 v[152:155], v[32:35], v[112:115], v[152:155]
	v_mfma_f32_16x16x32_f16 v[156:159], v[32:35], v[120:123], v[156:159]
	v_mfma_f32_16x16x32_f16 v[160:163], v[32:35], v[128:131], v[160:163]
	s_waitcnt lgkmcnt(0)
	ds_write_b32 v6, v6 offset:64
	ds_read_b32 v9, v7 offset:64
	v_mul_f32_e32 v244, v132, v136
	v_mul_f32_e32 v250, v133, v137
	v_mul_f32_e64 v245, -v136, v136
	v_mul_f32_e64 v251, -v137, v137
	v_add_f32_e32 v246, v132, v136
	v_add_f32_e32 v252, v133, v137
	v_fma_f32 v245, -v132, v132, v245
	v_fma_f32 v251, -v133, v133, v251
	v_fma_f32 v247, v10, v246, v11
	v_fma_f32 v253, v10, v252, v11
	v_fma_f32 v246, v13, v144, v14
	v_fma_f32 v252, v13, v145, v14
	v_fma_f32 v248, v12, v140, v245
	v_fma_f32 v254, v12, v141, v251
	v_fma_f32 v249, 2.0, v244, v247
	v_fma_f32 v255, 2.0, v250, v253
	v_sub_f32_e32 v247, v247, v245
	v_sub_f32_e32 v253, v253, v251
	v_fma_f32 v246, -2.0, v244, v246
	v_fma_f32 v252, -2.0, v250, v252
	v_mul_f32_e32 v247, v247, v248
	v_mul_f32_e32 v253, v253, v254
	v_rcp_f32_e32 v247, v247
	v_rcp_f32_e32 v253, v253
	v_mul_f32_e32 v249, v249, v246
	v_mul_f32_e32 v255, v255, v252
	v_fma_f32 v19, v249, v247, v19
	v_fma_f32 v19, v255, v253, v19
	v_mul_f32_e32 v244, v134, v138
	v_mul_f32_e32 v250, v135, v139
	v_mul_f32_e64 v245, -v138, v138
	v_mul_f32_e64 v251, -v139, v139
	v_add_f32_e32 v246, v134, v138
	v_add_f32_e32 v252, v135, v139
	v_fma_f32 v245, -v134, v134, v245
	v_fma_f32 v251, -v135, v135, v251
	v_fma_f32 v247, v10, v246, v11
	v_fma_f32 v253, v10, v252, v11
	v_fma_f32 v246, v13, v146, v14
	v_fma_f32 v252, v13, v147, v14
	v_fma_f32 v248, v12, v142, v245
	v_fma_f32 v254, v12, v143, v251
	v_fma_f32 v249, 2.0, v244, v247
	v_fma_f32 v255, 2.0, v250, v253
	v_sub_f32_e32 v247, v247, v245
	v_sub_f32_e32 v253, v253, v251
	v_fma_f32 v246, -2.0, v244, v246
	v_fma_f32 v252, -2.0, v250, v252
	v_mul_f32_e32 v247, v247, v248
	v_mul_f32_e32 v253, v253, v254
	v_rcp_f32_e32 v247, v247
	v_rcp_f32_e32 v253, v253
	v_mul_f32_e32 v249, v249, v246
	v_mul_f32_e32 v255, v255, v252
	v_fma_f32 v20, v249, v247, v20
	v_fma_f32 v20, v255, v253, v20
	v_mfma_f32_16x16x32_f16 v[132:135], v[24:27], v[104:107], 0
	v_mfma_f32_16x16x32_f16 v[136:139], v[24:27], v[112:115], 0
	v_mfma_f32_16x16x32_f16 v[140:143], v[24:27], v[120:123], v[0:3]
	v_mfma_f32_16x16x32_f16 v[144:147], v[24:27], v[128:131], 0
	s_waitcnt lgkmcnt(0)
	v_cmp_ne_u32_e32 vcc, 0, v9
	s_cbranch_vccnz .Lq_go_2
.Lq_spin_2:
	s_sleep 1
	ds_read_b32 v9, v7 offset:64
	s_waitcnt lgkmcnt(0)
	v_cmp_eq_u32_e32 vcc, 0, v9
	s_cbranch_vccnz .Lq_spin_2
.Lq_go_2:
	ds_read_b128 v[228:231], v5 offset:32768
	ds_read_b128 v[232:235], v5 offset:33280
	ds_read_b128 v[236:239], v5 offset:33792
	ds_read_b128 v[240:243], v5 offset:34304
	v_mul_f32_e32 v244, v148, v152
	v_mul_f32_e32 v250, v149, v153
	v_mul_f32_e64 v245, -v152, v152
	v_mul_f32_e64 v251, -v153, v153
	v_add_f32_e32 v246, v148, v152
	v_add_f32_e32 v252, v149, v153
	v_fma_f32 v245, -v148, v148, v245
	v_fma_f32 v251, -v149, v149, v251
	v_fma_f32 v247, v10, v246, v11
	v_fma_f32 v253, v10, v252, v11
	v_fma_f32 v246, v13, v160, v14
	v_fma_f32 v252, v13, v161, v14
	v_fma_f32 v248, v12, v156, v245
	v_fma_f32 v254, v12, v157, v251
	v_fma_f32 v249, 2.0, v244, v247
	v_fma_f32 v255, 2.0, v250, v253
	v_sub_f32_e32 v247, v247, v245
	v_sub_f32_e32 v253, v253, v251
	v_fma_f32 v246, -2.0, v244, v246
	v_fma_f32 v252, -2.0, v250, v252
	v_mul_f32_e32 v247, v247, v248
	v_mul_f32_e32 v253, v253, v254
	v_rcp_f32_e32 v247, v247
	v_rcp_f32_e32 v253, v253
	v_mul_f32_e32 v249, v249, v246
	v_mul_f32_e32 v255, v255, v252
	v_fma_f32 v19, v249, v247, v19
	v_fma_f32 v19, v255, v253, v19
	v_mul_f32_e32 v244, v150, v154
	v_mul_f32_e32 v250, v151, v155
	v_mul_f32_e64 v245, -v154, v154
	v_mul_f32_e64 v251, -v155, v155
	v_add_f32_e32 v246, v150, v154
	v_add_f32_e32 v252, v151, v155
	v_fma_f32 v245, -v150, v150, v245
	v_fma_f32 v251, -v151, v151, v251
	v_fma_f32 v247, v10, v246, v11
	v_fma_f32 v253, v10, v252, v11
	v_fma_f32 v246, v13, v162, v14
	v_fma_f32 v252, v13, v163, v14
	v_fma_f32 v248, v12, v158, v245
	v_fma_f32 v254, v12, v159, v251
	v_fma_f32 v249, 2.0, v244, v247
	v_fma_f32 v255, 2.0, v250, v253
	v_sub_f32_e32 v247, v247, v245
	v_sub_f32_e32 v253, v253, v251
	v_fma_f32 v246, -2.0, v244, v246
	v_fma_f32 v252, -2.0, v250, v252
	v_mul_f32_e32 v247, v247, v248
	v_mul_f32_e32 v253, v253, v254
	v_rcp_f32_e32 v247, v247
	v_rcp_f32_e32 v253, v253
	v_mul_f32_e32 v249, v249, v246
	v_mul_f32_e32 v255, v255, v252
	v_fma_f32 v20, v249, v247, v20
	v_fma_f32 v20, v255, v253, v20
	s_waitcnt lgkmcnt(0)
	v_mfma_f32_16x16x32_f16 v[148:151], v[28:31], v[228:231], 0
	v_mfma_f32_16x16x32_f16 v[152:155], v[28:31], v[232:235], 0
	v_mfma_f32_16x16x32_f16 v[156:159], v[28:31], v[236:239], v[0:3]
	v_mfma_f32_16x16x32_f16 v[160:163], v[28:31], v[240:243], 0
	v_mfma_f32_16x16x32_f16 v[148:151], v[32:35], v[100:103], v[148:151]
	v_mfma_f32_16x16x32_f16 v[152:155], v[32:35], v[108:111], v[152:155]
	v_mfma_f32_16x16x32_f16 v[156:159], v[32:35], v[116:119], v[156:159]
	v_mfma_f32_16x16x32_f16 v[160:163], v[32:35], v[124:127], v[160:163]
	v_mul_f32_e32 v244, v132, v136
	v_mul_f32_e32 v250, v133, v137
	v_mul_f32_e64 v245, -v136, v136
	v_mul_f32_e64 v251, -v137, v137
	v_add_f32_e32 v246, v132, v136
	v_add_f32_e32 v252, v133, v137
	v_fma_f32 v245, -v132, v132, v245
	v_fma_f32 v251, -v133, v133, v251
	v_fma_f32 v247, v10, v246, v11
	v_fma_f32 v253, v10, v252, v11
	v_fma_f32 v246, v13, v144, v14
	v_fma_f32 v252, v13, v145, v14
	v_fma_f32 v248, v12, v140, v245
	v_fma_f32 v254, v12, v141, v251
	v_fma_f32 v249, 2.0, v244, v247
	v_fma_f32 v255, 2.0, v250, v253
	v_sub_f32_e32 v247, v247, v245
	v_sub_f32_e32 v253, v253, v251
	v_fma_f32 v246, -2.0, v244, v246
	v_fma_f32 v252, -2.0, v250, v252
	v_mul_f32_e32 v247, v247, v248
	v_mul_f32_e32 v253, v253, v254
	v_rcp_f32_e32 v247, v247
	v_rcp_f32_e32 v253, v253
	v_mul_f32_e32 v249, v249, v246
	v_mul_f32_e32 v255, v255, v252
	v_fma_f32 v19, v249, v247, v19
	v_fma_f32 v19, v255, v253, v19
	v_mul_f32_e32 v244, v134, v138
	v_mul_f32_e32 v250, v135, v139
	v_mul_f32_e64 v245, -v138, v138
	v_mul_f32_e64 v251, -v139, v139
	v_add_f32_e32 v246, v134, v138
	v_add_f32_e32 v252, v135, v139
	v_fma_f32 v245, -v134, v134, v245
	v_fma_f32 v251, -v135, v135, v251
	v_fma_f32 v247, v10, v246, v11
	v_fma_f32 v253, v10, v252, v11
	v_fma_f32 v246, v13, v146, v14
	v_fma_f32 v252, v13, v147, v14
	v_fma_f32 v248, v12, v142, v245
	v_fma_f32 v254, v12, v143, v251
	v_fma_f32 v249, 2.0, v244, v247
	v_fma_f32 v255, 2.0, v250, v253
	v_sub_f32_e32 v247, v247, v245
	v_sub_f32_e32 v253, v253, v251
	v_fma_f32 v246, -2.0, v244, v246
	v_fma_f32 v252, -2.0, v250, v252
	v_mul_f32_e32 v247, v247, v248
	v_mul_f32_e32 v253, v253, v254
	v_rcp_f32_e32 v247, v247
	v_rcp_f32_e32 v253, v253
	v_mul_f32_e32 v249, v249, v246
	v_mul_f32_e32 v255, v255, v252
	v_fma_f32 v20, v249, v247, v20
	v_fma_f32 v20, v255, v253, v20
	v_mul_f32_e32 v244, v148, v152
	v_mul_f32_e32 v250, v149, v153
	v_mul_f32_e64 v245, -v152, v152
	v_mul_f32_e64 v251, -v153, v153
	v_add_f32_e32 v246, v148, v152
	v_add_f32_e32 v252, v149, v153
	v_fma_f32 v245, -v148, v148, v245
	v_fma_f32 v251, -v149, v149, v251
	v_fma_f32 v247, v10, v246, v11
	v_fma_f32 v253, v10, v252, v11
	v_fma_f32 v246, v13, v160, v14
	v_fma_f32 v252, v13, v161, v14
	v_fma_f32 v248, v12, v156, v245
	v_fma_f32 v254, v12, v157, v251
	v_fma_f32 v249, 2.0, v244, v247
	v_fma_f32 v255, 2.0, v250, v253
	v_sub_f32_e32 v247, v247, v245
	v_sub_f32_e32 v253, v253, v251
	v_fma_f32 v246, -2.0, v244, v246
	v_fma_f32 v252, -2.0, v250, v252
	v_mul_f32_e32 v247, v247, v248
	v_mul_f32_e32 v253, v253, v254
	v_rcp_f32_e32 v247, v247
	v_rcp_f32_e32 v253, v253
	v_mul_f32_e32 v249, v249, v246
	v_mul_f32_e32 v255, v255, v252
	v_mul_f32_e32 v249, v249, v247
	v_mul_f32_e32 v255, v255, v253
	v_fma_f32 v19, v249, v15, v19
	v_fma_f32 v19, v255, v16, v19
	v_mul_f32_e32 v244, v150, v154
	v_mul_f32_e32 v250, v151, v155
	v_mul_f32_e64 v245, -v154, v154
	v_mul_f32_e64 v251, -v155, v155
	v_add_f32_e32 v246, v150, v154
	v_add_f32_e32 v252, v151, v155
	v_fma_f32 v245, -v150, v150, v245
	v_fma_f32 v251, -v151, v151, v251
	v_fma_f32 v247, v10, v246, v11
	v_fma_f32 v253, v10, v252, v11
	v_fma_f32 v246, v13, v162, v14
	v_fma_f32 v252, v13, v163, v14
	v_fma_f32 v248, v12, v158, v245
	v_fma_f32 v254, v12, v159, v251
	v_fma_f32 v249, 2.0, v244, v247
	v_fma_f32 v255, 2.0, v250, v253
	v_sub_f32_e32 v247, v247, v245
	v_sub_f32_e32 v253, v253, v251
	v_fma_f32 v246, -2.0, v244, v246
	v_fma_f32 v252, -2.0, v250, v252
	v_mul_f32_e32 v247, v247, v248
	v_mul_f32_e32 v253, v253, v254
	v_rcp_f32_e32 v247, v247
	v_rcp_f32_e32 v253, v253
	v_mul_f32_e32 v249, v249, v246
	v_mul_f32_e32 v255, v255, v252
	v_mul_f32_e32 v249, v249, v247
	v_mul_f32_e32 v255, v255, v253
	v_fma_f32 v20, v249, v17, v20
	v_fma_f32 v20, v255, v18, v20
	s_waitcnt vmcnt(0)
	v_lshlrev_b32_e32 v23, 4, v8
	v_add_u32_e32 v23, s96, v23
	ds_read_b128 v[164:167], v23 offset:0
	ds_read_b128 v[168:171], v23 offset:1024
	ds_read_b128 v[172:175], v23 offset:2048
	ds_read_b128 v[176:179], v23 offset:3072
	ds_read_b128 v[180:183], v23 offset:4096
	ds_read_b128 v[184:187], v23 offset:5120
	ds_read_b128 v[188:191], v23 offset:6144
	ds_read_b128 v[192:195], v23 offset:7168
	s_waitcnt lgkmcnt(0)
	v_cvt_pk_f16_f32 v100, v164, v168
	v_cvt_pk_f16_f32 v116, v180, v184
	v_pk_add_f16 v100, v100, -0.5 op_sel_hi:[1,0]
	v_pk_add_f16 v116, v116, -0.5 op_sel_hi:[1,0]
	v_pk_mul_f16 v132, v116, v116
	v_pk_mul_f16 v148, v100, v116
	v_pk_fma_f16 v132, v100, v100, v132
	v_cvt_pk_f16_f32 v104, v165, v169
	v_cvt_pk_f16_f32 v120, v181, v185
	v_pk_add_f16 v104, v104, -0.5 op_sel_hi:[1,0]
	v_pk_add_f16 v120, v120, -0.5 op_sel_hi:[1,0]
	v_pk_mul_f16 v136, v120, v120
	v_pk_mul_f16 v152, v104, v120
	v_pk_fma_f16 v136, v104, v104, v136
	v_cvt_pk_f16_f32 v108, v166, v170
	v_cvt_pk_f16_f32 v124, v182, v186
	v_pk_add_f16 v108, v108, -0.5 op_sel_hi:[1,0]
	v_pk_add_f16 v124, v124, -0.5 op_sel_hi:[1,0]
	v_pk_mul_f16 v140, v124, v124
	v_pk_mul_f16 v156, v108, v124
	v_pk_fma_f16 v140, v108, v108, v140
	v_cvt_pk_f16_f32 v112, v167, v171
	v_cvt_pk_f16_f32 v128, v183, v187
	v_pk_add_f16 v112, v112, -0.5 op_sel_hi:[1,0]
	v_pk_add_f16 v128, v128, -0.5 op_sel_hi:[1,0]
	v_pk_mul_f16 v144, v128, v128
	v_pk_mul_f16 v160, v112, v128
	v_pk_fma_f16 v144, v112, v112, v144
	v_cvt_pk_f16_f32 v101, v172, v176
	v_cvt_pk_f16_f32 v117, v188, v192
	v_pk_add_f16 v101, v101, -0.5 op_sel_hi:[1,0]
	v_pk_add_f16 v117, v117, -0.5 op_sel_hi:[1,0]
	v_pk_mul_f16 v133, v117, v117
	v_pk_mul_f16 v149, v101, v117
	v_pk_fma_f16 v133, v101, v101, v133
	v_cvt_pk_f16_f32 v105, v173, v177
	v_cvt_pk_f16_f32 v121, v189, v193
	v_pk_add_f16 v105, v105, -0.5 op_sel_hi:[1,0]
	v_pk_add_f16 v121, v121, -0.5 op_sel_hi:[1,0]
	v_pk_mul_f16 v137, v121, v121
	v_pk_mul_f16 v153, v105, v121
	v_pk_fma_f16 v137, v105, v105, v137
	v_cvt_pk_f16_f32 v109, v174, v178
	v_cvt_pk_f16_f32 v125, v190, v194
	v_pk_add_f16 v109, v109, -0.5 op_sel_hi:[1,0]
	v_pk_add_f16 v125, v125, -0.5 op_sel_hi:[1,0]
	v_pk_mul_f16 v141, v125, v125
	v_pk_mul_f16 v157, v109, v125
	v_pk_fma_f16 v141, v109, v109, v141
	v_cvt_pk_f16_f32 v113, v175, v179
	v_cvt_pk_f16_f32 v129, v191, v195
	v_pk_add_f16 v113, v113, -0.5 op_sel_hi:[1,0]
	v_pk_add_f16 v129, v129, -0.5 op_sel_hi:[1,0]
	v_pk_mul_f16 v145, v129, v129
	v_pk_mul_f16 v161, v113, v129
	v_pk_fma_f16 v145, v113, v113, v145
	v_xor_b32_e32 v23, 32, v8
	v_lshlrev_b32_e32 v23, 2, v23
	ds_bpermute_b32 v102, v23, v100
	ds_bpermute_b32 v103, v23, v101
	ds_bpermute_b32 v106, v23, v104
	ds_bpermute_b32 v107, v23, v105
	ds_bpermute_b32 v110, v23, v108
	ds_bpermute_b32 v111, v23, v109
	ds_bpermute_b32 v114, v23, v112
	ds_bpermute_b32 v115, v23, v113
	s_waitcnt lgkmcnt(0)
	ds_bpermute_b32 v118, v23, v116
	ds_bpermute_b32 v119, v23, v117
	ds_bpermute_b32 v122, v23, v120
	ds_bpermute_b32 v123, v23, v121
	ds_bpermute_b32 v126, v23, v124
	ds_bpermute_b32 v127, v23, v125
	ds_bpermute_b32 v130, v23, v128
	ds_bpermute_b32 v131, v23, v129
	s_waitcnt lgkmcnt(0)
	ds_bpermute_b32 v134, v23, v132
	ds_bpermute_b32 v135, v23, v133
	ds_bpermute_b32 v138, v23, v136
	ds_bpermute_b32 v139, v23, v137
	ds_bpermute_b32 v142, v23, v140
	ds_bpermute_b32 v143, v23, v141
	ds_bpermute_b32 v146, v23, v144
	ds_bpermute_b32 v147, v23, v145
	s_waitcnt lgkmcnt(0)
	ds_bpermute_b32 v150, v23, v148
	ds_bpermute_b32 v151, v23, v149
	ds_bpermute_b32 v154, v23, v152
	ds_bpermute_b32 v155, v23, v153
	ds_bpermute_b32 v158, v23, v156
	ds_bpermute_b32 v159, v23, v157
	ds_bpermute_b32 v162, v23, v160
	ds_bpermute_b32 v163, v23, v161
	s_waitcnt lgkmcnt(0)
	v_mfma_f32_16x16x32_f16 v[196:199], v[36:39], v[28:31], 0
	v_mfma_f32_16x16x32_f16 v[200:203], v[40:43], v[28:31], 0
	v_mfma_f32_16x16x32_f16 v[204:207], v[44:47], v[28:31], 0
	v_mfma_f32_16x16x32_f16 v[208:211], v[48:51], v[28:31], 0
	v_mfma_f32_16x16x32_f16 v[196:199], v[100:103], v[32:35], v[196:199]
	v_mfma_f32_16x16x32_f16 v[200:203], v[104:107], v[32:35], v[200:203]
	v_mfma_f32_16x16x32_f16 v[204:207], v[108:111], v[32:35], v[204:207]
	v_mfma_f32_16x16x32_f16 v[208:211], v[112:115], v[32:35], v[208:211]
	v_mfma_f32_16x16x32_f16 v[212:215], v[52:55], v[28:31], 0
	v_mfma_f32_16x16x32_f16 v[216:219], v[56:59], v[28:31], 0
	v_mfma_f32_16x16x32_f16 v[220:223], v[60:63], v[28:31], 0
	v_mfma_f32_16x16x32_f16 v[224:227], v[64:67], v[28:31], 0
	v_mfma_f32_16x16x32_f16 v[212:215], v[116:119], v[32:35], v[212:215]
	v_mfma_f32_16x16x32_f16 v[216:219], v[120:123], v[32:35], v[216:219]
	v_mfma_f32_16x16x32_f16 v[220:223], v[124:127], v[32:35], v[220:223]
	v_mfma_f32_16x16x32_f16 v[224:227], v[128:131], v[32:35], v[224:227]
	v_cvt_pk_f16_f32 v164, v196, v200
	v_cvt_pk_f16_f32 v165, v204, v208
	v_cvt_pk_f16_f32 v166, v197, v201
	v_cvt_pk_f16_f32 v167, v205, v209
	v_cvt_pk_f16_f32 v168, v198, v202
	v_cvt_pk_f16_f32 v169, v206, v210
	v_cvt_pk_f16_f32 v170, v199, v203
	v_cvt_pk_f16_f32 v171, v207, v211
	v_mfma_f32_16x16x32_f16 v[196:199], v[68:71], v[28:31], 0
	v_mfma_f32_16x16x32_f16 v[200:203], v[72:75], v[28:31], 0
	v_mfma_f32_16x16x32_f16 v[204:207], v[76:79], v[28:31], 0
	v_mfma_f32_16x16x32_f16 v[208:211], v[80:83], v[28:31], 0
	v_mfma_f32_16x16x32_f16 v[196:199], v[132:135], v[32:35], v[196:199]
	v_mfma_f32_16x16x32_f16 v[200:203], v[136:139], v[32:35], v[200:203]
	v_mfma_f32_16x16x32_f16 v[204:207], v[140:143], v[32:35], v[204:207]
	v_mfma_f32_16x16x32_f16 v[208:211], v[144:147], v[32:35], v[208:211]
	v_cvt_pk_f16_f32 v172, v212, v216
	v_cvt_pk_f16_f32 v173, v220, v224
	v_cvt_pk_f16_f32 v174, v213, v217
	v_cvt_pk_f16_f32 v175, v221, v225
	v_cvt_pk_f16_f32 v176, v214, v218
	v_cvt_pk_f16_f32 v177, v222, v226
	v_cvt_pk_f16_f32 v178, v215, v219
	v_cvt_pk_f16_f32 v179, v223, v227
	v_mfma_f32_16x16x32_f16 v[212:215], v[84:87], v[28:31], 0
	v_mfma_f32_16x16x32_f16 v[216:219], v[88:91], v[28:31], 0
	v_mfma_f32_16x16x32_f16 v[220:223], v[92:95], v[28:31], 0
	v_mfma_f32_16x16x32_f16 v[224:227], v[96:99], v[28:31], 0
	v_mfma_f32_16x16x32_f16 v[212:215], v[148:151], v[32:35], v[212:215]
	v_mfma_f32_16x16x32_f16 v[216:219], v[152:155], v[32:35], v[216:219]
	v_mfma_f32_16x16x32_f16 v[220:223], v[156:159], v[32:35], v[220:223]
	v_mfma_f32_16x16x32_f16 v[224:227], v[160:163], v[32:35], v[224:227]
	v_cvt_pk_f16_f32 v180, v196, v200
	v_cvt_pk_f16_f32 v181, v204, v208
	v_cvt_pk_f16_f32 v182, v197, v201
	v_cvt_pk_f16_f32 v183, v205, v209
	v_cvt_pk_f16_f32 v184, v198, v202
	v_cvt_pk_f16_f32 v185, v206, v210
	v_cvt_pk_f16_f32 v186, v199, v203
	v_cvt_pk_f16_f32 v187, v207, v211
	v_cvt_pk_f16_f32 v188, v212, v216
	v_cvt_pk_f16_f32 v189, v220, v224
	v_cvt_pk_f16_f32 v190, v213, v217
	v_cvt_pk_f16_f32 v191, v221, v225
	v_cvt_pk_f16_f32 v192, v214, v218
	v_cvt_pk_f16_f32 v193, v222, v226
	v_cvt_pk_f16_f32 v194, v215, v219
	v_cvt_pk_f16_f32 v195, v223, v227
	s_mov_b64 exec, s[38:39]
	ds_write_b128 v4, v[168:171] offset:49152
	ds_write_b128 v4, v[176:179] offset:49664
	ds_write_b128 v4, v[184:187] offset:50176
	ds_write_b128 v4, v[192:195] offset:50688
	s_mov_b64 exec, -1
	v_mfma_f32_16x16x32_f16 v[196:199], v[24:27], v[164:167], 0
	v_mfma_f32_16x16x32_f16 v[200:203], v[24:27], v[172:175], 0
	v_mfma_f32_16x16x32_f16 v[204:207], v[24:27], v[180:183], v[0:3]
	v_mfma_f32_16x16x32_f16 v[208:211], v[24:27], v[188:191], 0
	v_mfma_f32_16x16x32_f16 v[212:215], v[28:31], v[164:167], 0
	v_mfma_f32_16x16x32_f16 v[216:219], v[28:31], v[172:175], 0
	v_mfma_f32_16x16x32_f16 v[220:223], v[28:31], v[180:183], v[0:3]
	v_mfma_f32_16x16x32_f16 v[224:227], v[28:31], v[188:191], 0
	v_mfma_f32_16x16x32_f16 v[212:215], v[32:35], v[168:171], v[212:215]
	v_mfma_f32_16x16x32_f16 v[216:219], v[32:35], v[176:179], v[216:219]
	v_mfma_f32_16x16x32_f16 v[220:223], v[32:35], v[184:187], v[220:223]
	v_mfma_f32_16x16x32_f16 v[224:227], v[32:35], v[192:195], v[224:227]
	s_waitcnt lgkmcnt(0)
	ds_write_b32 v6, v6 offset:96
	ds_read_b32 v9, v7 offset:96
	v_mul_f32_e32 v244, v196, v200
	v_mul_f32_e32 v250, v197, v201
	v_mul_f32_e64 v245, -v200, v200
	v_mul_f32_e64 v251, -v201, v201
	v_add_f32_e32 v246, v196, v200
	v_add_f32_e32 v252, v197, v201
	v_fma_f32 v245, -v196, v196, v245
	v_fma_f32 v251, -v197, v197, v251
	v_fma_f32 v247, v10, v246, v11
	v_fma_f32 v253, v10, v252, v11
	v_fma_f32 v246, v13, v208, v14
	v_fma_f32 v252, v13, v209, v14
	v_fma_f32 v248, v12, v204, v245
	v_fma_f32 v254, v12, v205, v251
	v_fma_f32 v249, 2.0, v244, v247
	v_fma_f32 v255, 2.0, v250, v253
	v_sub_f32_e32 v247, v247, v245
	v_sub_f32_e32 v253, v253, v251
	v_fma_f32 v246, -2.0, v244, v246
	v_fma_f32 v252, -2.0, v250, v252
	v_mul_f32_e32 v247, v247, v248
	v_mul_f32_e32 v253, v253, v254
	v_rcp_f32_e32 v247, v247
	v_rcp_f32_e32 v253, v253
	v_mul_f32_e32 v249, v249, v246
	v_mul_f32_e32 v255, v255, v252
	v_fma_f32 v21, v249, v247, v21
	v_fma_f32 v21, v255, v253, v21
	v_mul_f32_e32 v244, v198, v202
	v_mul_f32_e32 v250, v199, v203
	v_mul_f32_e64 v245, -v202, v202
	v_mul_f32_e64 v251, -v203, v203
	v_add_f32_e32 v246, v198, v202
	v_add_f32_e32 v252, v199, v203
	v_fma_f32 v245, -v198, v198, v245
	v_fma_f32 v251, -v199, v199, v251
	v_fma_f32 v247, v10, v246, v11
	v_fma_f32 v253, v10, v252, v11
	v_fma_f32 v246, v13, v210, v14
	v_fma_f32 v252, v13, v211, v14
	v_fma_f32 v248, v12, v206, v245
	v_fma_f32 v254, v12, v207, v251
	v_fma_f32 v249, 2.0, v244, v247
	v_fma_f32 v255, 2.0, v250, v253
	v_sub_f32_e32 v247, v247, v245
	v_sub_f32_e32 v253, v253, v251
	v_fma_f32 v246, -2.0, v244, v246
	v_fma_f32 v252, -2.0, v250, v252
	v_mul_f32_e32 v247, v247, v248
	v_mul_f32_e32 v253, v253, v254
	v_rcp_f32_e32 v247, v247
	v_rcp_f32_e32 v253, v253
	v_mul_f32_e32 v249, v249, v246
	v_mul_f32_e32 v255, v255, v252
	v_fma_f32 v22, v249, v247, v22
	v_fma_f32 v22, v255, v253, v22
	v_mfma_f32_16x16x32_f16 v[196:199], v[24:27], v[168:171], 0
	v_mfma_f32_16x16x32_f16 v[200:203], v[24:27], v[176:179], 0
	v_mfma_f32_16x16x32_f16 v[204:207], v[24:27], v[184:187], v[0:3]
	v_mfma_f32_16x16x32_f16 v[208:211], v[24:27], v[192:195], 0
	s_waitcnt lgkmcnt(0)
	v_cmp_ne_u32_e32 vcc, 0, v9
	s_cbranch_vccnz .Lq_go_3
.Lq_spin_3:
	s_sleep 1
	ds_read_b32 v9, v7 offset:96
	s_waitcnt lgkmcnt(0)
	v_cmp_eq_u32_e32 vcc, 0, v9
	s_cbranch_vccnz .Lq_spin_3
.Lq_go_3:
	ds_read_b128 v[228:231], v5 offset:49152
	ds_read_b128 v[232:235], v5 offset:49664
	ds_read_b128 v[236:239], v5 offset:50176
	ds_read_b128 v[240:243], v5 offset:50688
	v_mul_f32_e32 v244, v212, v216
	v_mul_f32_e32 v250, v213, v217
	v_mul_f32_e64 v245, -v216, v216
	v_mul_f32_e64 v251, -v217, v217
	v_add_f32_e32 v246, v212, v216
	v_add_f32_e32 v252, v213, v217
	v_fma_f32 v245, -v212, v212, v245
	v_fma_f32 v251, -v213, v213, v251
	v_fma_f32 v247, v10, v246, v11
	v_fma_f32 v253, v10, v252, v11
	v_fma_f32 v246, v13, v224, v14
	v_fma_f32 v252, v13, v225, v14
	v_fma_f32 v248, v12, v220, v245
	v_fma_f32 v254, v12, v221, v251
	v_fma_f32 v249, 2.0, v244, v247
	v_fma_f32 v255, 2.0, v250, v253
	v_sub_f32_e32 v247, v247, v245
	v_sub_f32_e32 v253, v253, v251
	v_fma_f32 v246, -2.0, v244, v246
	v_fma_f32 v252, -2.0, v250, v252
	v_mul_f32_e32 v247, v247, v248
	v_mul_f32_e32 v253, v253, v254
	v_rcp_f32_e32 v247, v247
	v_rcp_f32_e32 v253, v253
	v_mul_f32_e32 v249, v249, v246
	v_mul_f32_e32 v255, v255, v252
	v_fma_f32 v21, v249, v247, v21
	v_fma_f32 v21, v255, v253, v21
	v_mul_f32_e32 v244, v214, v218
	v_mul_f32_e32 v250, v215, v219
	v_mul_f32_e64 v245, -v218, v218
	v_mul_f32_e64 v251, -v219, v219
	v_add_f32_e32 v246, v214, v218
	v_add_f32_e32 v252, v215, v219
	v_fma_f32 v245, -v214, v214, v245
	v_fma_f32 v251, -v215, v215, v251
	v_fma_f32 v247, v10, v246, v11
	v_fma_f32 v253, v10, v252, v11
	v_fma_f32 v246, v13, v226, v14
	v_fma_f32 v252, v13, v227, v14
	v_fma_f32 v248, v12, v222, v245
	v_fma_f32 v254, v12, v223, v251
	v_fma_f32 v249, 2.0, v244, v247
	v_fma_f32 v255, 2.0, v250, v253
	v_sub_f32_e32 v247, v247, v245
	v_sub_f32_e32 v253, v253, v251
	v_fma_f32 v246, -2.0, v244, v246
	v_fma_f32 v252, -2.0, v250, v252
	v_mul_f32_e32 v247, v247, v248
	v_mul_f32_e32 v253, v253, v254
	v_rcp_f32_e32 v247, v247
	v_rcp_f32_e32 v253, v253
	v_mul_f32_e32 v249, v249, v246
	v_mul_f32_e32 v255, v255, v252
	v_fma_f32 v22, v249, v247, v22
	v_fma_f32 v22, v255, v253, v22
	s_waitcnt lgkmcnt(0)
	v_mfma_f32_16x16x32_f16 v[212:215], v[28:31], v[228:231], 0
	v_mfma_f32_16x16x32_f16 v[216:219], v[28:31], v[232:235], 0
	v_mfma_f32_16x16x32_f16 v[220:223], v[28:31], v[236:239], v[0:3]
	v_mfma_f32_16x16x32_f16 v[224:227], v[28:31], v[240:243], 0
	v_mfma_f32_16x16x32_f16 v[212:215], v[32:35], v[164:167], v[212:215]
	v_mfma_f32_16x16x32_f16 v[216:219], v[32:35], v[172:175], v[216:219]
	v_mfma_f32_16x16x32_f16 v[220:223], v[32:35], v[180:183], v[220:223]
	v_mfma_f32_16x16x32_f16 v[224:227], v[32:35], v[188:191], v[224:227]
	v_mul_f32_e32 v244, v196, v200
	v_mul_f32_e32 v250, v197, v201
	v_mul_f32_e64 v245, -v200, v200
	v_mul_f32_e64 v251, -v201, v201
	v_add_f32_e32 v246, v196, v200
	v_add_f32_e32 v252, v197, v201
	v_fma_f32 v245, -v196, v196, v245
	v_fma_f32 v251, -v197, v197, v251
	v_fma_f32 v247, v10, v246, v11
	v_fma_f32 v253, v10, v252, v11
	v_fma_f32 v246, v13, v208, v14
	v_fma_f32 v252, v13, v209, v14
	v_fma_f32 v248, v12, v204, v245
	v_fma_f32 v254, v12, v205, v251
	v_fma_f32 v249, 2.0, v244, v247
	v_fma_f32 v255, 2.0, v250, v253
	v_sub_f32_e32 v247, v247, v245
	v_sub_f32_e32 v253, v253, v251
	v_fma_f32 v246, -2.0, v244, v246
	v_fma_f32 v252, -2.0, v250, v252
	v_mul_f32_e32 v247, v247, v248
	v_mul_f32_e32 v253, v253, v254
	v_rcp_f32_e32 v247, v247
	v_rcp_f32_e32 v253, v253
	v_mul_f32_e32 v249, v249, v246
	v_mul_f32_e32 v255, v255, v252
	v_fma_f32 v21, v249, v247, v21
	v_fma_f32 v21, v255, v253, v21
	v_mul_f32_e32 v244, v198, v202
	v_mul_f32_e32 v250, v199, v203
	v_mul_f32_e64 v245, -v202, v202
	v_mul_f32_e64 v251, -v203, v203
	v_add_f32_e32 v246, v198, v202
	v_add_f32_e32 v252, v199, v203
	v_fma_f32 v245, -v198, v198, v245
	v_fma_f32 v251, -v199, v199, v251
	v_fma_f32 v247, v10, v246, v11
	v_fma_f32 v253, v10, v252, v11
	v_fma_f32 v246, v13, v210, v14
	v_fma_f32 v252, v13, v211, v14
	v_fma_f32 v248, v12, v206, v245
	v_fma_f32 v254, v12, v207, v251
	v_fma_f32 v249, 2.0, v244, v247
	v_fma_f32 v255, 2.0, v250, v253
	v_sub_f32_e32 v247, v247, v245
	v_sub_f32_e32 v253, v253, v251
	v_fma_f32 v246, -2.0, v244, v246
	v_fma_f32 v252, -2.0, v250, v252
	v_mul_f32_e32 v247, v247, v248
	v_mul_f32_e32 v253, v253, v254
	v_rcp_f32_e32 v247, v247
	v_rcp_f32_e32 v253, v253
	v_mul_f32_e32 v249, v249, v246
	v_mul_f32_e32 v255, v255, v252
	v_fma_f32 v22, v249, v247, v22
	v_fma_f32 v22, v255, v253, v22
	v_mul_f32_e32 v244, v212, v216
	v_mul_f32_e32 v250, v213, v217
	v_mul_f32_e64 v245, -v216, v216
	v_mul_f32_e64 v251, -v217, v217
	v_add_f32_e32 v246, v212, v216
	v_add_f32_e32 v252, v213, v217
	v_fma_f32 v245, -v212, v212, v245
	v_fma_f32 v251, -v213, v213, v251
	v_fma_f32 v247, v10, v246, v11
	v_fma_f32 v253, v10, v252, v11
	v_fma_f32 v246, v13, v224, v14
	v_fma_f32 v252, v13, v225, v14
	v_fma_f32 v248, v12, v220, v245
	v_fma_f32 v254, v12, v221, v251
	v_fma_f32 v249, 2.0, v244, v247
	v_fma_f32 v255, 2.0, v250, v253
	v_sub_f32_e32 v247, v247, v245
	v_sub_f32_e32 v253, v253, v251
	v_fma_f32 v246, -2.0, v244, v246
	v_fma_f32 v252, -2.0, v250, v252
	v_mul_f32_e32 v247, v247, v248
	v_mul_f32_e32 v253, v253, v254
	v_rcp_f32_e32 v247, v247
	v_rcp_f32_e32 v253, v253
	v_mul_f32_e32 v249, v249, v246
	v_mul_f32_e32 v255, v255, v252
	v_mul_f32_e32 v249, v249, v247
	v_mul_f32_e32 v255, v255, v253
	v_fma_f32 v21, v249, v15, v21
	v_fma_f32 v21, v255, v16, v21
	v_mul_f32_e32 v244, v214, v218
	v_mul_f32_e32 v250, v215, v219
	v_mul_f32_e64 v245, -v218, v218
	v_mul_f32_e64 v251, -v219, v219
	v_add_f32_e32 v246, v214, v218
	v_add_f32_e32 v252, v215, v219
	v_fma_f32 v245, -v214, v214, v245
	v_fma_f32 v251, -v215, v215, v251
	v_fma_f32 v247, v10, v246, v11
	v_fma_f32 v253, v10, v252, v11
	v_fma_f32 v246, v13, v226, v14
	v_fma_f32 v252, v13, v227, v14
	v_fma_f32 v248, v12, v222, v245
	v_fma_f32 v254, v12, v223, v251
	v_fma_f32 v249, 2.0, v244, v247
	v_fma_f32 v255, 2.0, v250, v253
	v_sub_f32_e32 v247, v247, v245
	v_sub_f32_e32 v253, v253, v251
	v_fma_f32 v246, -2.0, v244, v246
	v_fma_f32 v252, -2.0, v250, v252
	v_mul_f32_e32 v247, v247, v248
	v_mul_f32_e32 v253, v253, v254
	v_rcp_f32_e32 v247, v247
	v_rcp_f32_e32 v253, v253
	v_mul_f32_e32 v249, v249, v246
	v_mul_f32_e32 v255, v255, v252
	v_mul_f32_e32 v249, v249, v247
	v_mul_f32_e32 v255, v255, v253
	v_fma_f32 v22, v249, v17, v22
	v_fma_f32 v22, v255, v18, v22
	v_add_f32_e32 v19, v19, v20
	v_add_f32_e32 v21, v21, v22
	v_and_b32_e32 v23, 15, v8
	s_cmp_eq_u32 s15, 7
	s_cselect_b32 s23, 6, 16
	v_cmp_gt_u32_e32 vcc, s23, v23
	s_nop 1
	v_cndmask_b32_e32 v21, 0, v21, vcc
	v_add_f32_e32 v19, v19, v21
	s_nop 1
	v_add_f32_dpp v19, v19, v19 quad_perm:[1,0,3,2] row_mask:0xf bank_mask:0xf
	s_nop 1
	v_add_f32_dpp v19, v19, v19 quad_perm:[2,3,0,1] row_mask:0xf bank_mask:0xf
	s_nop 1
	v_add_f32_dpp v19, v19, v19 row_half_mirror row_mask:0xf bank_mask:0xf
	s_nop 1
	v_add_f32_dpp v19, v19, v19 row_mirror row_mask:0xf bank_mask:0xf
	s_nop 0
	v_readlane_b32 s40, v19, 0
	v_readlane_b32 s41, v19, 16
	v_readlane_b32 s42, v19, 32
	v_readlane_b32 s43, v19, 48
	s_lshl_b32 s24, s2, 3
	s_add_u32 s24, s24, s12
	s_lshl_b32 s24, s24, 2
	v_mov_b32_e32 v19, s40
	v_add_f32_e32 v19, s41, v19
	v_add_f32_e32 v19, s42, v19
	v_add_f32_e32 v19, s43, v19
	v_mov_b32_e32 v9, s24
	v_cmp_eq_u32_e32 vcc, 0, v8
	s_nop 1
	s_and_saveexec_b64 s[30:31], vcc
	global_store_dword v9, v19, s[10:11]
	s_endpgm

	.amdhsa_kernel _Z9ssim_mainPKfS0_S0_Pf
		.amdhsa_group_segment_fixed_size 145536
		.amdhsa_private_segment_fixed_size 0
		.amdhsa_kernarg_size 32
		.amdhsa_user_sgpr_count 2
		.amdhsa_user_sgpr_dispatch_ptr 0
		.amdhsa_user_sgpr_queue_ptr 0
		.amdhsa_user_sgpr_kernarg_segment_ptr 1
		.amdhsa_user_sgpr_dispatch_id 0
		.amdhsa_user_sgpr_kernarg_preload_length 0
		.amdhsa_user_sgpr_kernarg_preload_offset 0
		.amdhsa_user_sgpr_private_segment_size 0
		.amdhsa_uses_dynamic_stack 0
		.amdhsa_enable_private_segment 0
		.amdhsa_system_sgpr_workgroup_id_x 1
		.amdhsa_system_sgpr_workgroup_id_y 0
		.amdhsa_system_sgpr_workgroup_id_z 0
		.amdhsa_system_sgpr_workgroup_info 0
		.amdhsa_system_vgpr_workitem_id 0
		.amdhsa_next_free_vgpr 256
		.amdhsa_next_free_sgpr 100
		.amdhsa_accum_offset 256
		.amdhsa_reserve_vcc 1
		.amdhsa_float_round_mode_32 0
		.amdhsa_float_round_mode_16_64 0
		.amdhsa_float_denorm_mode_32 3
		.amdhsa_float_denorm_mode_16_64 3
		.amdhsa_dx10_clamp 1
		.amdhsa_ieee_mode 1
		.amdhsa_fp16_overflow 0
		.amdhsa_tg_split 0
		.amdhsa_exception_fp_ieee_invalid_op 0
		.amdhsa_exception_fp_denorm_src 0
		.amdhsa_exception_fp_ieee_div_zero 0
		.amdhsa_exception_fp_ieee_overflow 0
		.amdhsa_exception_fp_ieee_underflow 0
		.amdhsa_exception_fp_ieee_inexact 0
		.amdhsa_exception_int_div_zero 0
	.end_amdhsa_kernel
